# speedup vs baseline: 1.0057x; 1.0057x over previous
.LBB3_32:
	s_barrier
	v_accvgpr_read_b32 v140, a72
	v_lshlrev_b64 v[142:143], 2, v[94:95]
	v_lshlrev_b64 v[144:145], 2, v[96:97]
	v_lshlrev_b64 v[146:147], 2, v[98:99]
	v_lshlrev_b64 v[148:149], 2, v[100:101]
	s_add_u32 s52, s10, 0x800000
	s_addc_u32 s53, s11, 0
	v_add_u32_e32 v150, 0x0, v140
	v_lshl_add_u64 v[152:153], s[52:53], 0, v[142:143]
	s_nop 0
	v_readfirstlane_b32 s44, v150
	s_mov_b32 m0, s44
	s_nop 0
	global_load_lds_dwordx4 v[152:153], off nt
	v_add_u32_e32 v150, 0x0, v90
	v_lshl_add_u64 v[152:153], s[52:53], 0, v[144:145]
	s_nop 0
	v_readfirstlane_b32 s44, v150
	s_mov_b32 m0, s44
	s_nop 0
	global_load_lds_dwordx4 v[152:153], off nt
	v_add_u32_e32 v150, 0x0, v91
	v_lshl_add_u64 v[152:153], s[52:53], 0, v[146:147]
	s_nop 0
	v_readfirstlane_b32 s44, v150
	s_mov_b32 m0, s44
	s_nop 0
	global_load_lds_dwordx4 v[152:153], off nt
	v_add_u32_e32 v150, 0x0, v119
	v_lshl_add_u64 v[152:153], s[52:53], 0, v[148:149]
	s_nop 0
	v_readfirstlane_b32 s44, v150
	s_mov_b32 m0, s44
	s_nop 0
	global_load_lds_dwordx4 v[152:153], off nt
	s_add_u32 s52, s10, 0xc00000
	s_addc_u32 s53, s11, 0
	v_add_u32_e32 v150, 0x7000, v140
	v_lshl_add_u64 v[152:153], s[52:53], 0, v[142:143]
	s_nop 0
	v_readfirstlane_b32 s44, v150
	s_mov_b32 m0, s44
	s_nop 0
	global_load_lds_dwordx4 v[152:153], off nt
	v_add_u32_e32 v150, 0x7000, v90
	v_lshl_add_u64 v[152:153], s[52:53], 0, v[144:145]
	s_nop 0
	v_readfirstlane_b32 s44, v150
	s_mov_b32 m0, s44
	s_nop 0
	global_load_lds_dwordx4 v[152:153], off nt
	v_add_u32_e32 v150, 0x7000, v91
	v_lshl_add_u64 v[152:153], s[52:53], 0, v[146:147]
	s_nop 0
	v_readfirstlane_b32 s44, v150
	s_mov_b32 m0, s44
	s_nop 0
	global_load_lds_dwordx4 v[152:153], off nt
	v_add_u32_e32 v150, 0x7000, v119
	v_lshl_add_u64 v[152:153], s[52:53], 0, v[148:149]
	s_nop 0
	v_readfirstlane_b32 s44, v150
	s_mov_b32 m0, s44
	s_nop 0
	global_load_lds_dwordx4 v[152:153], off nt
	s_add_u32 s52, s10, 0x1000000
	s_addc_u32 s53, s11, 0
	v_add_u32_e32 v150, 0xe000, v140
	v_lshl_add_u64 v[152:153], s[52:53], 0, v[142:143]
	s_nop 0
	v_readfirstlane_b32 s44, v150
	s_mov_b32 m0, s44
	s_nop 0
	global_load_lds_dwordx4 v[152:153], off nt
	v_add_u32_e32 v150, 0xe000, v90
	v_lshl_add_u64 v[152:153], s[52:53], 0, v[144:145]
	s_nop 0
	v_readfirstlane_b32 s44, v150
	s_mov_b32 m0, s44
	s_nop 0
	global_load_lds_dwordx4 v[152:153], off nt
	v_add_u32_e32 v150, 0xe000, v91
	v_lshl_add_u64 v[152:153], s[52:53], 0, v[146:147]
	s_nop 0
	v_readfirstlane_b32 s44, v150
	s_mov_b32 m0, s44
	s_nop 0
	global_load_lds_dwordx4 v[152:153], off nt
	v_add_u32_e32 v150, 0xe000, v119
	v_lshl_add_u64 v[152:153], s[52:53], 0, v[148:149]
	s_nop 0
	v_readfirstlane_b32 s44, v150
	s_mov_b32 m0, s44
	s_nop 0
	global_load_lds_dwordx4 v[152:153], off nt
	v_lshl_add_u32 v0, v120, 5, s22
	v_or_b32_e32 v1, s23, v121
	s_movk_i32 s0, 0x7f
	v_lshl_or_b32 v7, v93, 1, v0
	s_movk_i32 s1, 0x7e
	s_nop 15
	s_nop 15
	v_cmp_eq_u32_e64 s[4:5], s1, v7
	s_nop 7
	v_cmp_gt_u32_e32 vcc, s0, v1
	v_accvgpr_read_b32 v5, a14
	v_cmp_eq_u32_e64 s[0:1], 0, v1
	v_or_b32_e32 v4, v93, v7
	v_cmp_eq_u32_e64 s[2:3], 0, v4
	v_cndmask_b32_e64 v14, v5, 0, s[0:1]
	v_accvgpr_read_b32 v5, a13
	v_cndmask_b32_e64 v22, v5, 0, s[0:1]
	v_accvgpr_read_b32 v5, a12
	v_cndmask_b32_e64 v116, v5, 0, s[0:1]
	v_accvgpr_read_b32 v5, a49
	v_cndmask_b32_e32 v16, 0, v5, vcc
	v_accvgpr_read_b32 v5, a48
	v_cndmask_b32_e32 v28, 0, v5, vcc
	v_accvgpr_read_b32 v5, a30
	v_cndmask_b32_e64 v10, v5, 0, s[0:1]
	v_accvgpr_read_b32 v5, a29
	v_cndmask_b32_e64 v24, v5, 0, s[0:1]
	v_accvgpr_read_b32 v5, a28
	v_cndmask_b32_e64 v42, v5, 0, s[0:1]
	v_accvgpr_read_b32 v5, a57
	v_cndmask_b32_e32 v20, 0, v5, vcc
	v_accvgpr_read_b32 v5, a56
	v_cndmask_b32_e32 v38, 0, v5, vcc
	v_accvgpr_read_b32 v5, a6
	v_cndmask_b32_e64 v15, v5, 0, s[0:1]
	v_accvgpr_read_b32 v5, a5
	v_cndmask_b32_e64 v23, v5, 0, s[0:1]
	v_accvgpr_read_b32 v5, a4
	v_cndmask_b32_e64 v117, v5, 0, s[0:1]
	v_accvgpr_read_b32 v5, a41
	v_cndmask_b32_e32 v17, 0, v5, vcc
	v_accvgpr_read_b32 v5, a40
	v_cndmask_b32_e32 v29, 0, v5, vcc
	v_accvgpr_read_b32 v5, a17
	v_cndmask_b32_e64 v37, v5, 0, s[0:1]
	v_accvgpr_read_b32 v5, a16
	v_cndmask_b32_e64 v47, v5, 0, s[0:1]
	v_accvgpr_read_b32 v5, a52
	v_cndmask_b32_e32 v45, 0, v5, vcc
	v_accvgpr_read_b32 v5, a68
	v_cndmask_b32_e32 v12, 0, v5, vcc
	v_accvgpr_read_b32 v5, a0
	s_or_b64 s[8:9], s[2:3], s[0:1]
	v_cmp_eq_u32_e64 s[6:7], 15, v93
	v_accvgpr_read_b32 v11, a8
	v_cndmask_b32_e64 v112, v5, 0, s[8:9]
	v_accvgpr_read_b32 v4, a67
	v_mov_b32_e32 v5, 0x90
	s_and_b64 s[4:5], s[6:7], s[4:5]
	v_mov_b64_e32 v[40:41], v[16:17]
	v_cndmask_b32_e64 v16, v11, 0, s[2:3]
	v_cndmask_b32_e64 v11, 12, v5, s[6:7]
	v_cndmask_b32_e64 v61, v4, 0, s[4:5]
	v_accvgpr_read_b32 v4, a61
	s_or_b64 s[6:7], s[4:5], s[0:1]
	v_cndmask_b32_e64 v87, v4, 0, s[6:7]
	v_accvgpr_read_b32 v4, a60
	v_cndmask_b32_e64 v86, v4, 0, s[6:7]
	v_accvgpr_read_b32 v4, a65
	v_cndmask_b32_e64 v5, v4, 0, s[4:5]
	v_accvgpr_read_b32 v4, a64
	v_cndmask_b32_e64 v4, v4, 0, s[4:5]
	s_lshl_b32 s14, s18, 2
	v_mov_b64_e32 v[32:33], v[4:5]
	v_lshl_or_b32 v4, v122, 18, s14
	v_mov_b32_e32 v5, 0
	v_mov_b64_e32 v[62:63], v[14:15]
	v_lshl_add_u64 v[14:15], s[12:13], 0, v[4:5]
	v_lshlrev_b32_e32 v4, 7, v1
	v_lshl_add_u64 v[14:15], v[4:5], 2, v[14:15]
	v_lshlrev_b32_e32 v4, 2, v7
	v_mul_u32_u24_e32 v1, 24, v122
	v_lshl_add_u64 v[54:55], v[14:15], 0, v[4:5]
	v_mbcnt_lo_u32_b32 v138, -1, 0
	v_mbcnt_hi_u32_b32 v138, -1, v138
	v_and_b32_e32 v138, 1, v138
	v_mul_u32_u24_e32 v138, 0xfff8, v138
	v_add_u32_e32 v138, 0xffff0000, v138
	v_mov_b32_e32 v139, -1
	v_lshl_add_u64 v[134:135], v[54:55], 0, v[138:139]
	s_mov_b32 s28, 0x55555555
	s_mov_b32 s29, 0x55555555
	s_mov_b32 s30, 0xaaaaaaaa
	s_mov_b32 s31, 0xaaaaaaaa
	v_or_b32_e32 v1, v1, v121
	v_lshlrev_b32_e32 v4, 7, v120
	s_movk_i32 s12, 0x120
	v_mad_u32_u24 v1, v1, s12, v4
	s_add_u32 s12, s10, 0x800000
	v_accvgpr_read_b32 v7, a72
	v_mov_b64_e32 v[80:81], v[28:29]
	s_addc_u32 s13, s11, 0
	v_lshlrev_b64 v[28:29], 2, v[94:95]
	v_readfirstlane_b32 s14, v7
	v_add_u32_e32 v7, 0, v90
	v_lshl_add_u64 v[4:5], s[12:13], 0, v[28:29]
	s_mov_b32 m0, s14
	v_lshlrev_b64 v[30:31], 2, v[96:97]
	v_readfirstlane_b32 s14, v7
	v_mov_b32_e32 v14, v7
	v_add_u32_e32 v7, 0, v91
	s_waitcnt lgkmcnt(0)
	v_lshlrev_b64 v[56:57], 2, v[98:99]
	v_mov_b32_e32 v19, v7
	v_lshlrev_b64 v[58:59], 2, v[100:101]
	v_add_u32_e32 v7, 0, v119
	v_accvgpr_read_b32 v25, a72
	v_mov_b32_e32 v21, v7
	v_lshl_add_u32 v15, v93, 3, v1
	v_add_u32_e32 v1, v1, v11
	s_waitcnt vmcnt(16)
	v_accvgpr_write_b32 a12, v14
	v_mov_b64_e32 v[124:125], v[56:57]
	v_accvgpr_write_b32 a13, v19
	v_mov_b64_e32 v[126:127], v[58:59]
	v_accvgpr_write_b32 a16, v21
	s_waitcnt lgkmcnt(0)
	s_barrier
	v_add_u32_e32 v14, 0x16010, v15
	v_mov_b32_e32 v122, v15
	v_add_u32_e32 v15, 0x16000, v1
	ds_read_b64 v[64:65], v14
	ds_read_b64 v[66:67], v14 offset:288
	ds_read_b64 v[68:69], v14 offset:576
	ds_read_b64 v[76:77], v14 offset:1728
	ds_read_b64 v[78:79], v14 offset:2016
	ds_read_b64 v[4:5], v14 offset:2304
	ds_read_b64 v[84:85], v14 offset:3456
	ds_read_b64 v[74:75], v14 offset:3744
	ds_read_b64 v[88:89], v14 offset:4032
	ds_read_b64 v[100:101], v14 offset:5184
	ds_read_b64 v[106:107], v14 offset:5472
	ds_read_b64 v[120:121], v14 offset:5760
	ds_read_b32 v43, v15
	ds_read_b32 v19, v15 offset:288
	ds_read_b32 v39, v15 offset:576
	ds_read_b32 v25, v15 offset:1728
	ds_read_b32 v7, v15 offset:2016
	ds_read_b32 v21, v15 offset:2304
	ds_read_b32 v11, v15 offset:3456
	ds_read_b32 v35, v15 offset:3744
	ds_read_b32 v59, v15 offset:4032
	ds_read_b32 v57, v15 offset:5184
	ds_read_b32 v51, v15 offset:5472
	ds_read_b32 v49, v15 offset:5760
	s_waitcnt lgkmcnt(0)
	v_accvgpr_read_b32 v8, a26
	v_mov_b32_e32 v46, v43
	v_mov_b32_e32 v113, v65
	v_mov_b32_e32 v26, v19
	v_mov_b32_dpp v46, v65 row_shr:1 row_mask:0xf bank_mask:0xf
	v_pk_mul_f32 v[70:71], v[112:113], v[46:47]
	v_accvgpr_read_b32 v9, a22
	v_accvgpr_read_b32 v27, a36
	v_mov_b32_dpp v43, v64 row_shl:1 row_mask:0xf bank_mask:0xf
	v_mov_b32_dpp v26, v67 row_shr:1 row_mask:0xf bank_mask:0xf
	v_pk_fma_f32 v[70:71], v[64:65], v[116:117], v[70:71] op_sel_hi:[0,1,1]
	v_pk_mov_b32 v[64:65], v[64:65], v[86:87] op_sel:[1,0]
	v_mov_b32_e32 v17, v67
	v_mov_b64_e32 v[102:103], v[8:9]
	v_accvgpr_read_b32 v8, a25
	v_accvgpr_read_b32 v114, a24
	v_accvgpr_read_b32 v9, a21
	v_accvgpr_read_b32 v115, a20
	v_accvgpr_read_b32 v2, a32
	v_mov_b64_e32 v[82:83], v[30:31]
	v_pk_fma_f32 v[70:71], v[64:65], v[42:43], v[70:71]
	v_pk_mul_f32 v[64:65], v[16:17], v[26:27]
	v_mov_b64_e32 v[30:31], v[32:33]
	v_accvgpr_read_b32 v18, a44
	v_mov_b64_e32 v[104:105], v[8:9]
	v_cndmask_b32_e32 v9, 0, v2, vcc
	v_accvgpr_write_b32 a4, v14
	v_mov_b32_dpp v19, v66 row_shl:1 row_mask:0xf bank_mask:0xf
	v_pk_fma_f32 v[64:65], v[66:67], v[114:115], v[64:65] op_sel_hi:[0,1,1]
	v_pk_mov_b32 v[66:67], v[66:67], v[30:31] op_sel:[1,0]
	v_accvgpr_read_b32 v14, a69
	v_mov_b32_e32 v44, v39
	v_mov_b32_e32 v60, v1
	v_pk_fma_f32 v[66:67], v[66:67], v[18:19], v[64:65]
	v_cndmask_b32_e32 v14, 0, v14, vcc
	v_cndmask_b32_e64 v0, v9, 0, s[2:3]
	v_mov_b32_dpp v44, v69 row_shr:1 row_mask:0xf bank_mask:0xf
	v_pk_add_f32 v[70:71], v[70:71], 0 op_sel_hi:[1,0]
	v_mov_b32_e32 v1, v69
	v_accvgpr_write_b32 a0, v15
	v_cndmask_b32_e64 v15, v14, 0, s[4:5]
	v_cndmask_b32_e64 v14, v12, 0, s[4:5]
	v_pk_add_f32 v[66:67], v[70:71], v[66:67]
	v_pk_mul_f32 v[70:71], v[0:1], v[44:45]
	v_mov_b32_dpp v39, v68 row_shl:1 row_mask:0xf bank_mask:0xf
	v_pk_fma_f32 v[70:71], v[68:69], v[80:81], v[70:71] op_sel_hi:[0,1,1]
	v_pk_mov_b32 v[68:69], v[68:69], v[14:15] op_sel:[1,0]
	v_accvgpr_read_b32 v9, a1
	v_pk_fma_f32 v[68:69], v[68:69], v[38:39], v[70:71]
	v_mov_b32_e32 v36, v25
	v_cndmask_b32_e64 v64, v9, 0, s[8:9]
	v_pk_add_f32 v[66:67], v[66:67], v[68:69]
	v_mov_b32_dpp v36, v77 row_shr:1 row_mask:0xf bank_mask:0xf
	v_mov_b32_e32 v65, v77
	v_mov_b64_e32 v[108:109], v[22:23]
	v_accvgpr_read_b32 v9, a9
	v_mov_b32_e32 v128, v66
	v_mov_b32_e32 v129, v67
	v_mov_b32_e32 v12, v7
	v_pk_mul_f32 v[66:67], v[64:65], v[36:37]
	v_accvgpr_read_b32 v13, a37
	v_mov_b64_e32 v[72:73], v[28:29]
	v_cndmask_b32_e64 v28, v9, 0, s[2:3]
	v_mov_b32_dpp v25, v76 row_shl:1 row_mask:0xf bank_mask:0xf
	v_mov_b32_dpp v12, v79 row_shr:1 row_mask:0xf bank_mask:0xf
	v_pk_fma_f32 v[66:67], v[76:77], v[108:109], v[66:67] op_sel_hi:[0,1,1]
	v_mov_b32_e32 v76, v77
	v_mov_b32_e32 v77, v87
	v_mov_b32_e32 v29, v79
	v_pk_fma_f32 v[66:67], v[76:77], v[24:25], v[66:67]
	v_pk_mul_f32 v[76:77], v[28:29], v[12:13]
	v_accvgpr_read_b32 v6, a45
	v_accvgpr_read_b32 v2, a33
	v_mov_b32_dpp v7, v78 row_shl:1 row_mask:0xf bank_mask:0xf
	v_pk_fma_f32 v[76:77], v[78:79], v[104:105], v[76:77] op_sel_hi:[0,1,1]
	v_mov_b32_e32 v78, v79
	v_mov_b32_e32 v79, v31
	v_cndmask_b32_e32 v2, 0, v2, vcc
	v_accvgpr_read_b32 v50, a53
	v_pk_fma_f32 v[76:77], v[78:79], v[6:7], v[76:77]
	v_mov_b32_e32 v78, v21
	v_accvgpr_write_b32 a44, v80
	v_cndmask_b32_e32 v79, 0, v50, vcc
	v_cndmask_b32_e64 v52, v2, 0, s[2:3]
	v_mov_b32_dpp v78, v5 row_shr:1 row_mask:0xf bank_mask:0xf
	v_pk_add_f32 v[66:67], v[66:67], 0 op_sel_hi:[1,0]
	v_mov_b32_e32 v53, v5
	v_accvgpr_write_b32 a45, v81
	v_accvgpr_write_b32 a21, v15
	v_pk_add_f32 v[80:81], v[66:67], v[76:77]
	v_pk_mul_f32 v[66:67], v[52:53], v[78:79]
	v_accvgpr_write_b32 a24, v40
	v_accvgpr_read_b32 v2, a2
	v_mov_b32_dpp v21, v4 row_shl:1 row_mask:0xf bank_mask:0xf
	v_pk_fma_f32 v[66:67], v[4:5], v[40:41], v[66:67] op_sel_hi:[0,1,1]
	v_accvgpr_write_b32 a25, v41
	v_mov_b32_e32 v4, v5
	v_accvgpr_read_b32 v5, a21
	v_cndmask_b32_e64 v40, v2, 0, s[8:9]
	v_accvgpr_read_b32 v2, a62
	v_accvgpr_read_b32 v8, a18
	v_accvgpr_read_b32 v48, a63
	v_accvgpr_write_b32 a20, v14
	v_accvgpr_write_b32 a41, v23
	v_pk_fma_f32 v[4:5], v[4:5], v[20:21], v[66:67]
	s_mov_b64 s[12:13], 0x10000
	v_cndmask_b32_e64 v14, v2, 0, s[6:7]
	v_mov_b32_e32 v76, v11
	v_accvgpr_read_b32 v2, a10
	v_accvgpr_write_b32 a40, v22
	v_cndmask_b32_e64 v15, v48, 0, s[6:7]
	v_cndmask_b32_e64 v77, v8, 0, s[0:1]
	v_pk_add_f32 v[4:5], v[80:81], v[4:5]
	v_lshl_add_u64 v[136:137], v[134:135], 0, s[12:13]
	v_mov_b32_dpp v76, v85 row_shr:1 row_mask:0xf bank_mask:0xf
	v_mov_b32_e32 v41, v85
	v_cndmask_b32_e64 v22, v2, 0, s[2:3]
	v_mov_b32_e32 v2, v35
	v_accvgpr_read_b32 v1, a50
	v_accvgpr_read_b32 v3, a38
	s_mov_b64 s[32:33], vcc
	s_nop 1
	s_mov_b64 vcc, s[28:29]
	s_nop 0
	v_cndmask_b32_dpp v130, v4, v128, vcc quad_perm:[1,0,3,2] row_mask:0xf bank_mask:0xf
	v_cndmask_b32_dpp v131, v5, v129, vcc quad_perm:[1,0,3,2] row_mask:0xf bank_mask:0xf
	s_mov_b64 vcc, s[30:31]
	s_nop 0
	v_cndmask_b32_dpp v132, v128, v4, vcc quad_perm:[1,0,3,2] row_mask:0xf bank_mask:0xf
	v_cndmask_b32_dpp v133, v129, v5, vcc quad_perm:[1,0,3,2] row_mask:0xf bank_mask:0xf
	global_store_dwordx4 v[136:137], v[130:133], off sc0 sc1 nt
	s_nop 1
	s_mov_b64 vcc, s[32:33]
	v_mov_b64_e32 v[8:9], v[14:15]
	v_pk_mul_f32 v[4:5], v[40:41], v[76:77]
	v_mov_b64_e32 v[66:67], v[62:63]
	v_mov_b32_dpp v2, v75 row_shr:1 row_mask:0xf bank_mask:0xf
	v_mov_b32_e32 v23, v75
	v_cndmask_b32_e32 v62, 0, v1, vcc
	v_accvgpr_read_b32 v1, a42
	v_mov_b32_dpp v11, v84 row_shl:1 row_mask:0xf bank_mask:0xf
	v_pk_fma_f32 v[4:5], v[84:85], v[66:67], v[4:5] op_sel_hi:[0,1,1]
	v_pk_mov_b32 v[80:81], v[84:85], v[8:9] op_sel:[1,0]
	v_pk_mul_f32 v[84:85], v[22:23], v[2:3]
	v_accvgpr_read_b32 v2, a58
	v_cndmask_b32_e32 v63, 0, v1, vcc
	v_accvgpr_read_b32 v1, a70
	v_pk_fma_f32 v[80:81], v[80:81], v[10:11], v[4:5]
	v_accvgpr_read_b32 v4, a66
	v_cndmask_b32_e32 v58, 0, v2, vcc
	v_cndmask_b32_e32 v1, 0, v1, vcc
	v_accvgpr_read_b32 v2, a71
	v_cndmask_b32_e64 v8, v4, 0, s[4:5]
	v_cndmask_b32_e32 v2, 0, v2, vcc
	v_cndmask_b32_e64 v4, v1, 0, s[4:5]
	v_accvgpr_read_b32 v1, a34
	v_mov_b32_e32 v9, v61
	v_cndmask_b32_e64 v5, v2, 0, s[4:5]
	v_cndmask_b32_e32 v1, 0, v1, vcc
	v_accvgpr_read_b32 v2, a54
	v_mov_b32_e32 v92, v59
	v_accvgpr_read_b32 v34, a46
	v_mov_b32_dpp v35, v74 row_shl:1 row_mask:0xf bank_mask:0xf
	v_pk_fma_f32 v[84:85], v[74:75], v[102:103], v[84:85] op_sel_hi:[0,1,1]
	v_pk_mov_b32 v[74:75], v[74:75], v[8:9] op_sel:[1,0]
	v_cndmask_b32_e32 v93, 0, v2, vcc
	v_mov_b32_dpp v92, v89 row_shr:1 row_mask:0xf bank_mask:0xf
	v_cndmask_b32_e64 v96, v1, 0, s[2:3]
	v_mov_b32_e32 v97, v89
	v_accvgpr_read_b32 v1, a31
	v_pk_fma_f32 v[74:75], v[74:75], v[34:35], v[84:85]
	v_pk_mul_f32 v[84:85], v[96:97], v[92:93]
	v_accvgpr_write_b32 a8, v62
	v_cndmask_b32_e64 v56, v1, 0, s[0:1]
	v_accvgpr_read_b32 v1, a15
	v_pk_fma_f32 v[84:85], v[88:89], v[62:63], v[84:85] op_sel_hi:[0,1,1]
	v_accvgpr_write_b32 a9, v63
	v_cndmask_b32_e64 v62, v1, 0, s[0:1]
	v_accvgpr_read_b32 v1, a7
	v_cndmask_b32_e64 v63, v1, 0, s[0:1]
	v_accvgpr_read_b32 v1, a19
	v_pk_add_f32 v[80:81], v[80:81], 0 op_sel_hi:[1,0]
	v_mov_b32_dpp v59, v88 row_shl:1 row_mask:0xf bank_mask:0xf
	v_pk_mov_b32 v[88:89], v[88:89], v[4:5] op_sel:[1,0]
	v_cndmask_b32_e64 v95, v1, 0, s[0:1]
	v_accvgpr_read_b32 v1, a3
	v_accvgpr_write_b32 a36, v104
	v_pk_add_f32 v[80:81], v[80:81], v[74:75]
	v_pk_fma_f32 v[84:85], v[88:89], v[58:59], v[84:85]
	v_mov_b32_e32 v94, v57
	v_cndmask_b32_e64 v98, v1, 0, s[8:9]
	v_accvgpr_read_b32 v1, a11
	v_accvgpr_write_b32 a37, v105
	v_accvgpr_write_b32 a32, v102
	v_pk_add_f32 v[80:81], v[80:81], v[84:85]
	s_mov_b64 s[4:5], 0x20000
	v_mov_b32_dpp v94, v101 row_shr:1 row_mask:0xf bank_mask:0xf
	v_mov_b32_e32 v99, v101
	v_cndmask_b32_e64 v104, v1, 0, s[2:3]
	v_accvgpr_read_b32 v1, a59
	v_accvgpr_write_b32 a29, v15
	v_accvgpr_write_b32 a33, v103
	v_accvgpr_write_b32 a49, v5
	v_lshl_add_u64 v[84:85], v[54:55], 0, s[4:5]
	v_mov_b32_e32 v128, v80
	v_mov_b32_e32 v129, v81
	v_pk_mul_f32 v[80:81], v[98:99], v[94:95]
	v_mov_b32_e32 v102, v51
	v_cndmask_b32_e32 v48, 0, v1, vcc
	v_accvgpr_read_b32 v1, a51
	v_accvgpr_write_b32 a48, v4
	v_mov_b32_dpp v57, v100 row_shl:1 row_mask:0xf bank_mask:0xf
	v_pk_fma_f32 v[80:81], v[100:101], v[62:63], v[80:81] op_sel_hi:[0,1,1]
	v_mov_b32_e32 v84, v101
	v_accvgpr_read_b32 v85, a29
	v_accvgpr_read_b32 v103, a39
	v_mov_b32_dpp v102, v107 row_shr:1 row_mask:0xf bank_mask:0xf
	v_mov_b32_e32 v105, v107
	v_cndmask_b32_e32 v4, 0, v1, vcc
	v_accvgpr_read_b32 v1, a43
	v_pk_fma_f32 v[80:81], v[84:85], v[56:57], v[80:81]
	v_accvgpr_read_b32 v30, a27
	v_accvgpr_read_b32 v31, a23
	v_pk_mul_f32 v[84:85], v[104:105], v[102:103]
	v_cndmask_b32_e32 v5, 0, v1, vcc
	v_accvgpr_read_b32 v1, a35
	v_accvgpr_read_b32 v50, a47
	v_mov_b32_dpp v51, v106 row_shl:1 row_mask:0xf bank_mask:0xf
	v_pk_fma_f32 v[84:85], v[106:107], v[30:31], v[84:85] op_sel_hi:[0,1,1]
	v_mov_b32_e32 v106, v107
	v_mov_b32_e32 v107, v9
	v_cndmask_b32_e32 v1, 0, v1, vcc
	v_accvgpr_read_b32 v2, a55
	v_mov_b32_e32 v108, v49
	v_pk_fma_f32 v[84:85], v[106:107], v[50:51], v[84:85]
	v_pk_add_f32 v[80:81], v[80:81], 0 op_sel_hi:[1,0]
	v_cndmask_b32_e32 v109, 0, v2, vcc
	v_mov_b32_dpp v108, v121 row_shr:1 row_mask:0xf bank_mask:0xf
	v_cndmask_b32_e64 v110, v1, 0, s[2:3]
	v_mov_b32_e32 v111, v121
	v_pk_add_f32 v[80:81], v[80:81], v[84:85]
	v_pk_mul_f32 v[84:85], v[110:111], v[108:109]
	v_mov_b32_dpp v49, v120 row_shl:1 row_mask:0xf bank_mask:0xf
	v_pk_fma_f32 v[84:85], v[120:121], v[4:5], v[84:85] op_sel_hi:[0,1,1]
	v_mov_b32_e32 v120, v121
	v_accvgpr_read_b32 v121, a49
	v_pk_fma_f32 v[84:85], v[120:121], v[48:49], v[84:85]
	s_mov_b64 s[0:1], 0x30000
	v_pk_add_f32 v[80:81], v[80:81], v[84:85]
	v_lshl_add_u64 v[136:137], v[134:135], 0, s[0:1]
	v_add_u32_e32 v1, s17, v118
	s_add_u32 s0, s10, 0x1400000
	s_mov_b64 s[32:33], vcc
	s_nop 1
	s_mov_b64 vcc, s[28:29]
	s_nop 0
	v_cndmask_b32_dpp v130, v80, v128, vcc quad_perm:[1,0,3,2] row_mask:0xf bank_mask:0xf
	v_cndmask_b32_dpp v131, v81, v129, vcc quad_perm:[1,0,3,2] row_mask:0xf bank_mask:0xf
	s_mov_b64 vcc, s[30:31]
	s_nop 0
	v_cndmask_b32_dpp v132, v128, v80, vcc quad_perm:[1,0,3,2] row_mask:0xf bank_mask:0xf
	v_cndmask_b32_dpp v133, v129, v81, vcc quad_perm:[1,0,3,2] row_mask:0xf bank_mask:0xf
	global_store_dwordx4 v[136:137], v[130:133], off sc0 sc1 nt
	s_nop 1
	s_mov_b64 vcc, s[32:33]
	v_readfirstlane_b32 s2, v1
	s_addc_u32 s1, s11, 0
	v_add_u32_e32 v1, s17, v90
	s_waitcnt vmcnt(14)
	v_lshl_add_u64 v[80:81], s[0:1], 0, v[72:73]
	s_mov_b32 m0, s2
	v_readfirstlane_b32 s2, v1
	v_mov_b64_e32 v[74:75], v[82:83]
	v_add_u32_e32 v1, s17, v91
	s_waitcnt lgkmcnt(0)
	s_barrier
	global_load_lds_dwordx4 v[80:81], off nt
	v_lshl_add_u64 v[80:81], s[0:1], 0, v[74:75]
	s_mov_b32 m0, s2
	v_readfirstlane_b32 s2, v1
	v_add_u32_e32 v1, s17, v119
	global_load_lds_dwordx4 v[80:81], off nt
	v_lshl_add_u64 v[80:81], s[0:1], 0, v[124:125]
	s_mov_b32 m0, s2
	v_readfirstlane_b32 s2, v1
	global_load_lds_dwordx4 v[80:81], off nt
	v_lshl_add_u64 v[80:81], s[0:1], 0, v[126:127]
	s_mov_b32 m0, s2
	v_accvgpr_write_b32 a53, v33
	v_accvgpr_write_b32 a2, v62
	v_accvgpr_write_b32 a7, v5
	v_accvgpr_write_b32 a22, v124
	v_accvgpr_write_b32 a30, v126
	global_load_lds_dwordx4 v[80:81], off nt
	v_accvgpr_write_b32 a52, v32
	v_accvgpr_write_b32 a3, v63
	v_accvgpr_write_b32 a6, v4
	v_mov_b64_e32 v[32:33], v[72:73]
	v_accvgpr_write_b32 a23, v125
	v_accvgpr_write_b32 a31, v127
	v_add_u32_e32 v2, 0x1d010, v122
	v_accvgpr_write_b32 a10, v122
	v_add_u32_e32 v5, 0x1d000, v60
	v_mov_b32_e32 v4, v60
	ds_read_b64 v[62:63], v2
	ds_read_b64 v[60:61], v2 offset:288
	ds_read_b64 v[72:73], v2 offset:576
	ds_read_b64 v[70:71], v2 offset:1728
	ds_read_b64 v[68:69], v2 offset:2016
	ds_read_b64 v[82:83], v2 offset:2304
	ds_read_b64 v[80:81], v2 offset:3456
	ds_read_b64 v[84:85], v2 offset:3744
	ds_read_b64 v[126:127], v2 offset:4032
	ds_read_b64 v[124:125], v2 offset:5184
	ds_read_b64 v[122:123], v2 offset:5472
	ds_read_b64 v[120:121], v2 offset:5760
	ds_read_b32 v43, v5
	ds_read_b32 v19, v5 offset:288
	ds_read_b32 v39, v5 offset:576
	ds_read_b32 v25, v5 offset:1728
	ds_read_b32 v7, v5 offset:2016
	ds_read_b32 v21, v5 offset:2304
	ds_read_b32 v11, v5 offset:3456
	ds_read_b32 v35, v5 offset:3744
	ds_read_b32 v59, v5 offset:4032
	ds_read_b32 v57, v5 offset:5184
	ds_read_b32 v51, v5 offset:5472
	ds_read_b32 v49, v5 offset:5760
	s_waitcnt lgkmcnt(0)
	v_mov_b64_e32 v[100:101], v[86:87]
	v_mov_b32_e32 v46, v43
	v_mov_b32_e32 v113, v63
	v_mov_b32_e32 v26, v19
	v_mov_b32_dpp v46, v63 row_shr:1 row_mask:0xf bank_mask:0xf
	v_pk_mul_f32 v[88:89], v[112:113], v[46:47]
	v_mov_b32_dpp v43, v62 row_shl:1 row_mask:0xf bank_mask:0xf
	v_pk_fma_f32 v[88:89], v[62:63], v[116:117], v[88:89] op_sel_hi:[0,1,1]
	v_pk_mov_b32 v[62:63], v[62:63], v[100:101] op_sel:[1,0]
	v_mov_b32_dpp v26, v61 row_shr:1 row_mask:0xf bank_mask:0xf
	v_mov_b32_e32 v17, v61
	v_pk_fma_f32 v[62:63], v[62:63], v[42:43], v[88:89]
	v_pk_mul_f32 v[88:89], v[16:17], v[26:27]
	v_accvgpr_write_b32 a34, v16
	v_accvgpr_read_b32 v16, a52
	v_accvgpr_read_b32 v17, a53
	v_mov_b32_dpp v19, v60 row_shl:1 row_mask:0xf bank_mask:0xf
	v_pk_fma_f32 v[88:89], v[60:61], v[114:115], v[88:89] op_sel_hi:[0,1,1]
	v_pk_mov_b32 v[60:61], v[60:61], v[16:17] op_sel:[1,0]
	v_mov_b32_e32 v44, v39
	v_accvgpr_write_b32 a28, v14
	v_pk_fma_f32 v[60:61], v[60:61], v[18:19], v[88:89]
	v_pk_add_f32 v[62:63], v[62:63], 0 op_sel_hi:[1,0]
	v_mov_b32_dpp v44, v73 row_shr:1 row_mask:0xf bank_mask:0xf
	v_mov_b32_e32 v1, v73
	v_accvgpr_read_b32 v14, a44
	v_accvgpr_read_b32 v89, a21
	v_pk_add_f32 v[60:61], v[62:63], v[60:61]
	v_pk_mul_f32 v[62:63], v[0:1], v[44:45]
	v_accvgpr_read_b32 v15, a45
	v_accvgpr_read_b32 v88, a20
	v_mov_b32_dpp v39, v72 row_shl:1 row_mask:0xf bank_mask:0xf
	v_pk_fma_f32 v[62:63], v[72:73], v[14:15], v[62:63] op_sel_hi:[0,1,1]
	v_pk_mov_b32 v[72:73], v[72:73], v[88:89] op_sel:[1,0]
	v_mov_b32_e32 v36, v25
	v_pk_fma_f32 v[62:63], v[72:73], v[38:39], v[62:63]
	s_mov_b64 s[0:1], 0x400000
	v_pk_add_f32 v[60:61], v[60:61], v[62:63]
	v_mov_b32_dpp v36, v71 row_shr:1 row_mask:0xf bank_mask:0xf
	v_mov_b32_e32 v65, v71
	v_accvgpr_read_b32 v87, a41
	v_lshl_add_u64 v[62:63], v[54:55], 0, s[0:1]
	v_mov_b32_e32 v128, v60
	v_mov_b32_e32 v129, v61
	v_pk_mul_f32 v[60:61], v[64:65], v[36:37]
	v_accvgpr_read_b32 v86, a40
	v_mov_b32_e32 v12, v7
	v_mov_b32_dpp v25, v70 row_shl:1 row_mask:0xf bank_mask:0xf
	v_pk_fma_f32 v[60:61], v[70:71], v[86:87], v[60:61] op_sel_hi:[0,1,1]
	v_mov_b32_e32 v62, v71
	v_mov_b32_e32 v63, v101
	v_mov_b32_dpp v12, v69 row_shr:1 row_mask:0xf bank_mask:0xf
	v_mov_b32_e32 v29, v69
	v_accvgpr_read_b32 v107, a37
	v_pk_fma_f32 v[60:61], v[62:63], v[24:25], v[60:61]
	v_pk_mul_f32 v[62:63], v[28:29], v[12:13]
	v_accvgpr_read_b32 v106, a36
	v_mov_b32_dpp v7, v68 row_shl:1 row_mask:0xf bank_mask:0xf
	v_pk_fma_f32 v[62:63], v[68:69], v[106:107], v[62:63] op_sel_hi:[0,1,1]
	v_mov_b32_e32 v68, v69
	v_mov_b32_e32 v69, v17
	v_mov_b32_e32 v78, v21
	v_pk_fma_f32 v[62:63], v[68:69], v[6:7], v[62:63]
	v_pk_add_f32 v[60:61], v[60:61], 0 op_sel_hi:[1,0]
	v_mov_b32_dpp v78, v83 row_shr:1 row_mask:0xf bank_mask:0xf
	v_mov_b32_e32 v53, v83
	v_accvgpr_read_b32 v14, a24
	v_pk_add_f32 v[60:61], v[60:61], v[62:63]
	v_pk_mul_f32 v[62:63], v[52:53], v[78:79]
	v_accvgpr_read_b32 v15, a25
	v_mov_b32_dpp v21, v82 row_shl:1 row_mask:0xf bank_mask:0xf
	v_pk_fma_f32 v[62:63], v[82:83], v[14:15], v[62:63] op_sel_hi:[0,1,1]
	v_mov_b32_e32 v68, v83
	v_mov_b32_e32 v69, v89
	v_pk_fma_f32 v[62:63], v[68:69], v[20:21], v[62:63]
	v_mov_b32_e32 v76, v11
	v_pk_add_f32 v[60:61], v[60:61], v[62:63]
	s_mov_b64 s[0:1], 0x410000
	v_mov_b32_dpp v76, v81 row_shr:1 row_mask:0xf bank_mask:0xf
	v_mov_b32_e32 v41, v81
	v_lshl_add_u64 v[136:137], v[134:135], 0, s[0:1]
	s_nop 1
	s_mov_b64 vcc, s[28:29]
	s_nop 0
	v_cndmask_b32_dpp v130, v60, v128, vcc quad_perm:[1,0,3,2] row_mask:0xf bank_mask:0xf
	v_cndmask_b32_dpp v131, v61, v129, vcc quad_perm:[1,0,3,2] row_mask:0xf bank_mask:0xf
	s_mov_b64 vcc, s[30:31]
	s_nop 0
	v_cndmask_b32_dpp v132, v128, v60, vcc quad_perm:[1,0,3,2] row_mask:0xf bank_mask:0xf
	v_cndmask_b32_dpp v133, v129, v61, vcc quad_perm:[1,0,3,2] row_mask:0xf bank_mask:0xf
	global_store_dwordx4 v[136:137], v[130:133], off sc0 sc1 nt
	s_nop 1
	v_pk_mul_f32 v[60:61], v[40:41], v[76:77]
	v_accvgpr_write_b32 a36, v66
	v_pk_fma_f32 v[60:61], v[80:81], v[66:67], v[60:61] op_sel_hi:[0,1,1]
	v_accvgpr_write_b32 a37, v67
	v_accvgpr_read_b32 v67, a29
	v_accvgpr_write_b32 a5, v2
	v_accvgpr_write_b32 a38, v100
	v_accvgpr_read_b32 v66, a28
	v_mov_b32_e32 v2, v35
	v_accvgpr_write_b32 a39, v101
	v_mov_b32_dpp v11, v80 row_shl:1 row_mask:0xf bank_mask:0xf
	v_pk_mov_b32 v[62:63], v[80:81], v[66:67] op_sel:[1,0]
	v_mov_b32_dpp v2, v85 row_shr:1 row_mask:0xf bank_mask:0xf
	v_mov_b32_e32 v23, v85
	v_accvgpr_read_b32 v101, a33
	v_pk_fma_f32 v[60:61], v[62:63], v[10:11], v[60:61]
	v_pk_mul_f32 v[62:63], v[22:23], v[2:3]
	v_accvgpr_read_b32 v100, a32
	v_mov_b32_dpp v35, v84 row_shl:1 row_mask:0xf bank_mask:0xf
	v_pk_fma_f32 v[62:63], v[84:85], v[100:101], v[62:63] op_sel_hi:[0,1,1]
	v_pk_mov_b32 v[68:69], v[84:85], v[8:9] op_sel:[1,0]
	v_mov_b32_e32 v92, v59
	v_pk_fma_f32 v[62:63], v[68:69], v[34:35], v[62:63]
	v_pk_add_f32 v[60:61], v[60:61], 0 op_sel_hi:[1,0]
	v_mov_b32_dpp v92, v127 row_shr:1 row_mask:0xf bank_mask:0xf
	v_mov_b32_e32 v97, v127
	v_accvgpr_read_b32 v17, a9
	v_accvgpr_read_b32 v71, a49
	v_pk_add_f32 v[60:61], v[60:61], v[62:63]
	v_pk_mul_f32 v[62:63], v[96:97], v[92:93]
	v_accvgpr_read_b32 v16, a8
	v_accvgpr_read_b32 v70, a48
	v_mov_b32_dpp v59, v126 row_shl:1 row_mask:0xf bank_mask:0xf
	v_pk_fma_f32 v[62:63], v[126:127], v[16:17], v[62:63] op_sel_hi:[0,1,1]
	v_pk_mov_b32 v[68:69], v[126:127], v[70:71] op_sel:[1,0]
	v_mov_b32_e32 v94, v57
	v_pk_fma_f32 v[62:63], v[68:69], v[58:59], v[62:63]
	v_accvgpr_write_b32 a20, v28
	v_pk_add_f32 v[60:61], v[60:61], v[62:63]
	s_mov_b64 s[0:1], 0x420000
	v_mov_b32_dpp v94, v125 row_shr:1 row_mask:0xf bank_mask:0xf
	v_mov_b32_e32 v99, v125
	v_accvgpr_read_b32 v29, a3
	v_lshl_add_u64 v[62:63], v[54:55], 0, s[0:1]
	v_mov_b32_e32 v128, v60
	v_mov_b32_e32 v129, v61
	v_pk_mul_f32 v[60:61], v[98:99], v[94:95]
	v_accvgpr_read_b32 v28, a2
	v_mov_b32_e32 v102, v51
	v_mov_b32_dpp v57, v124 row_shl:1 row_mask:0xf bank_mask:0xf
	v_pk_fma_f32 v[60:61], v[124:125], v[28:29], v[60:61] op_sel_hi:[0,1,1]
	v_mov_b32_e32 v62, v125
	v_mov_b32_e32 v63, v67
	v_mov_b32_dpp v102, v123 row_shr:1 row_mask:0xf bank_mask:0xf
	v_mov_b32_e32 v105, v123
	v_pk_fma_f32 v[60:61], v[62:63], v[56:57], v[60:61]
	v_pk_mul_f32 v[62:63], v[104:105], v[102:103]
	v_mov_b32_dpp v51, v122 row_shl:1 row_mask:0xf bank_mask:0xf
	v_pk_fma_f32 v[62:63], v[122:123], v[30:31], v[62:63] op_sel_hi:[0,1,1]
	v_accvgpr_write_b32 a28, v30
	v_mov_b32_e32 v68, v123
	v_mov_b32_e32 v69, v9
	v_mov_b32_e32 v108, v49
	v_accvgpr_write_b32 a29, v31
	v_pk_fma_f32 v[62:63], v[68:69], v[50:51], v[62:63]
	v_pk_add_f32 v[60:61], v[60:61], 0 op_sel_hi:[1,0]
	v_mov_b32_dpp v108, v121 row_shr:1 row_mask:0xf bank_mask:0xf
	v_mov_b32_e32 v111, v121
	v_accvgpr_read_b32 v31, a7
	v_pk_add_f32 v[60:61], v[60:61], v[62:63]
	v_pk_mul_f32 v[62:63], v[110:111], v[108:109]
	v_accvgpr_read_b32 v30, a6
	v_mov_b32_dpp v49, v120 row_shl:1 row_mask:0xf bank_mask:0xf
	v_pk_fma_f32 v[62:63], v[120:121], v[30:31], v[62:63] op_sel_hi:[0,1,1]
	v_mov_b32_e32 v68, v121
	v_mov_b32_e32 v69, v71
	v_pk_fma_f32 v[62:63], v[68:69], v[48:49], v[62:63]
	s_mov_b64 s[0:1], 0x430000
	v_pk_add_f32 v[60:61], v[60:61], v[62:63]
	v_lshl_add_u64 v[136:137], v[134:135], 0, s[0:1]
	v_add_u32_e32 v1, s16, v118
	s_add_u32 s0, s10, 0x1800000
	v_accvgpr_write_b32 a26, v114
	s_nop 1
	s_mov_b64 vcc, s[28:29]
	s_nop 0
	v_cndmask_b32_dpp v130, v60, v128, vcc quad_perm:[1,0,3,2] row_mask:0xf bank_mask:0xf
	v_cndmask_b32_dpp v131, v61, v129, vcc quad_perm:[1,0,3,2] row_mask:0xf bank_mask:0xf
	s_mov_b64 vcc, s[30:31]
	s_nop 0
	v_cndmask_b32_dpp v132, v128, v60, vcc quad_perm:[1,0,3,2] row_mask:0xf bank_mask:0xf
	v_cndmask_b32_dpp v133, v129, v61, vcc quad_perm:[1,0,3,2] row_mask:0xf bank_mask:0xf
	global_store_dwordx4 v[136:137], v[130:133], off sc0 sc1 nt
	s_nop 1
	v_readfirstlane_b32 s2, v1
	s_addc_u32 s1, s11, 0
	v_add_u32_e32 v1, s16, v90
	v_accvgpr_write_b32 a18, v116
	v_accvgpr_write_b32 a27, v115
	s_waitcnt vmcnt(16)
	v_lshl_add_u64 v[60:61], s[0:1], 0, v[32:33]
	s_mov_b32 m0, s2
	v_readfirstlane_b32 s2, v1
	v_add_u32_e32 v1, s16, v91
	v_accvgpr_read_b32 v115, a23
	v_accvgpr_write_b32 a19, v117
	s_waitcnt lgkmcnt(0)
	s_barrier
	global_load_lds_dwordx4 v[60:61], off nt
	v_lshl_add_u64 v[60:61], s[0:1], 0, v[74:75]
	s_mov_b32 m0, s2
	v_readfirstlane_b32 s2, v1
	v_accvgpr_read_b32 v114, a22
	v_add_u32_e32 v1, s16, v119
	v_accvgpr_read_b32 v117, a31
	global_load_lds_dwordx4 v[60:61], off nt
	v_lshl_add_u64 v[60:61], s[0:1], 0, v[114:115]
	s_mov_b32 m0, s2
	v_readfirstlane_b32 s2, v1
	v_accvgpr_read_b32 v116, a30
	global_load_lds_dwordx4 v[60:61], off nt
	v_lshl_add_u64 v[60:61], s[0:1], 0, v[116:117]
	s_mov_b32 m0, s2
	v_accvgpr_write_b32 a1, v5
	global_load_lds_dwordx4 v[60:61], off nt
	v_accvgpr_read_b32 v5, a10
	v_add_u32_e32 v2, 16, v5
	ds_read_b64 v[60:61], v2
	ds_read_b64 v[62:63], v2 offset:288
	ds_read_b64 v[68:69], v2 offset:576
	ds_read_b64 v[70:71], v2 offset:1728
	ds_read_b64 v[72:73], v2 offset:2016
	ds_read_b64 v[82:83], v2 offset:2304
	ds_read_b64 v[80:81], v2 offset:3456
	ds_read_b64 v[84:85], v2 offset:3744
	ds_read_b64 v[124:125], v2 offset:4032
	ds_read_b64 v[122:123], v2 offset:5184
	ds_read_b64 v[120:121], v2 offset:5472
	ds_read_b64 v[90:91], v2 offset:5760
	ds_read_b32 v43, v4
	ds_read_b32 v19, v4 offset:288
	ds_read_b32 v39, v4 offset:576
	ds_read_b32 v25, v4 offset:1728
	ds_read_b32 v7, v4 offset:2016
	ds_read_b32 v21, v4 offset:2304
	ds_read_b32 v11, v4 offset:3456
	ds_read_b32 v35, v4 offset:3744
	ds_read_b32 v59, v4 offset:4032
	ds_read_b32 v57, v4 offset:5184
	ds_read_b32 v51, v4 offset:5472
	ds_read_b32 v49, v4 offset:5760
	s_waitcnt lgkmcnt(0)
	v_accvgpr_write_b32 a46, v88
	v_mov_b32_e32 v46, v43
	v_accvgpr_write_b32 a8, v8
	v_mov_b32_e32 v113, v61
	v_mov_b32_dpp v46, v61 row_shr:1 row_mask:0xf bank_mask:0xf
	v_accvgpr_mov_b32 a42, a52
	v_accvgpr_write_b32 a47, v89
	v_accvgpr_write_b32 a9, v9
	v_pk_mul_f32 v[88:89], v[112:113], v[46:47]
	v_accvgpr_write_b32 a40, v112
	v_accvgpr_read_b32 v8, a18
	v_accvgpr_read_b32 v113, a39
	v_accvgpr_mov_b32 a43, a53
	v_accvgpr_write_b32 a51, v33
	v_accvgpr_write_b32 a52, v74
	v_accvgpr_read_b32 v9, a19
	v_accvgpr_read_b32 v112, a38
	v_mov_b32_e32 v26, v19
	v_accvgpr_write_b32 a50, v32
	v_accvgpr_write_b32 a53, v75
	v_mov_b32_dpp v43, v60 row_shl:1 row_mask:0xf bank_mask:0xf
	v_pk_fma_f32 v[88:89], v[60:61], v[8:9], v[88:89] op_sel_hi:[0,1,1]
	v_pk_mov_b32 v[60:61], v[60:61], v[112:113] op_sel:[1,0]
	v_mov_b32_dpp v26, v63 row_shr:1 row_mask:0xf bank_mask:0xf
	v_accvgpr_read_b32 v32, a34
	v_mov_b32_e32 v33, v63
	v_accvgpr_read_b32 v127, a27
	v_accvgpr_read_b32 v75, a43
	v_pk_fma_f32 v[60:61], v[60:61], v[42:43], v[88:89]
	v_pk_mul_f32 v[88:89], v[32:33], v[26:27]
	v_accvgpr_read_b32 v126, a26
	v_accvgpr_read_b32 v74, a42
	v_mov_b32_dpp v19, v62 row_shl:1 row_mask:0xf bank_mask:0xf
	v_pk_fma_f32 v[88:89], v[62:63], v[126:127], v[88:89] op_sel_hi:[0,1,1]
	v_pk_mov_b32 v[62:63], v[62:63], v[74:75] op_sel:[1,0]
	v_mov_b32_e32 v44, v39
	v_accvgpr_mov_b32 a14, a48
	v_pk_fma_f32 v[62:63], v[62:63], v[18:19], v[88:89]
	v_pk_add_f32 v[60:61], v[60:61], 0 op_sel_hi:[1,0]
	v_mov_b32_dpp v44, v69 row_shr:1 row_mask:0xf bank_mask:0xf
	v_mov_b32_e32 v1, v69
	v_accvgpr_mov_b32 a15, a49
	v_pk_add_f32 v[60:61], v[60:61], v[62:63]
	v_pk_mul_f32 v[62:63], v[0:1], v[44:45]
	v_accvgpr_write_b32 a48, v0
	v_accvgpr_read_b32 v89, a45
	v_accvgpr_read_b32 v0, a46
	v_accvgpr_read_b32 v88, a44
	v_accvgpr_read_b32 v1, a47
	v_mov_b32_dpp v39, v68 row_shl:1 row_mask:0xf bank_mask:0xf
	v_pk_fma_f32 v[62:63], v[68:69], v[88:89], v[62:63] op_sel_hi:[0,1,1]
	v_pk_mov_b32 v[68:69], v[68:69], v[0:1] op_sel:[1,0]
	v_mov_b32_e32 v36, v25
	v_pk_fma_f32 v[62:63], v[68:69], v[38:39], v[62:63]
	s_mov_b64 s[0:1], 0x800000
	v_pk_add_f32 v[60:61], v[60:61], v[62:63]
	v_mov_b32_dpp v36, v71 row_shr:1 row_mask:0xf bank_mask:0xf
	v_mov_b32_e32 v65, v71
	v_lshl_add_u64 v[62:63], v[54:55], 0, s[0:1]
	v_mov_b32_e32 v128, v60
	v_mov_b32_e32 v129, v61
	v_pk_mul_f32 v[60:61], v[64:65], v[36:37]
	v_mov_b64_e32 v[118:119], v[86:87]
	v_mov_b32_e32 v12, v7
	v_accvgpr_write_b32 a24, v32
	v_mov_b32_dpp v25, v70 row_shl:1 row_mask:0xf bank_mask:0xf
	v_pk_fma_f32 v[60:61], v[70:71], v[118:119], v[60:61] op_sel_hi:[0,1,1]
	v_mov_b32_e32 v62, v71
	v_mov_b32_e32 v63, v113
	v_mov_b32_dpp v12, v73 row_shr:1 row_mask:0xf bank_mask:0xf
	v_accvgpr_read_b32 v32, a20
	v_mov_b32_e32 v33, v73
	v_pk_fma_f32 v[60:61], v[62:63], v[24:25], v[60:61]
	v_pk_mul_f32 v[62:63], v[32:33], v[12:13]
	v_mov_b32_dpp v7, v72 row_shl:1 row_mask:0xf bank_mask:0xf
	v_pk_fma_f32 v[62:63], v[72:73], v[106:107], v[62:63] op_sel_hi:[0,1,1]
	v_mov_b32_e32 v68, v73
	v_mov_b32_e32 v69, v75
	v_mov_b32_e32 v78, v21
	v_pk_fma_f32 v[62:63], v[68:69], v[6:7], v[62:63]
	v_pk_add_f32 v[60:61], v[60:61], 0 op_sel_hi:[1,0]
	v_mov_b32_dpp v78, v83 row_shr:1 row_mask:0xf bank_mask:0xf
	v_mov_b32_e32 v53, v83
	v_pk_add_f32 v[60:61], v[60:61], v[62:63]
	v_pk_mul_f32 v[62:63], v[52:53], v[78:79]
	v_mov_b32_dpp v21, v82 row_shl:1 row_mask:0xf bank_mask:0xf
	v_pk_fma_f32 v[62:63], v[82:83], v[14:15], v[62:63] op_sel_hi:[0,1,1]
	v_mov_b32_e32 v68, v83
	v_mov_b32_e32 v69, v1
	v_accvgpr_write_b32 a19, v15
	v_pk_fma_f32 v[62:63], v[68:69], v[20:21], v[62:63]
	v_mov_b32_e32 v76, v11
	v_accvgpr_write_b32 a18, v14
	v_pk_add_f32 v[60:61], v[60:61], v[62:63]
	s_mov_b64 s[0:1], 0x810000
	v_mov_b32_dpp v76, v81 row_shr:1 row_mask:0xf bank_mask:0xf
	v_mov_b32_e32 v41, v81
	v_accvgpr_read_b32 v14, a36
	v_accvgpr_write_b32 a6, v2
	v_lshl_add_u64 v[136:137], v[134:135], 0, s[0:1]
	s_nop 1
	s_mov_b64 vcc, s[28:29]
	s_nop 0
	v_cndmask_b32_dpp v130, v60, v128, vcc quad_perm:[1,0,3,2] row_mask:0xf bank_mask:0xf
	v_cndmask_b32_dpp v131, v61, v129, vcc quad_perm:[1,0,3,2] row_mask:0xf bank_mask:0xf
	s_mov_b64 vcc, s[30:31]
	s_nop 0
	v_cndmask_b32_dpp v132, v128, v60, vcc quad_perm:[1,0,3,2] row_mask:0xf bank_mask:0xf
	v_cndmask_b32_dpp v133, v129, v61, vcc quad_perm:[1,0,3,2] row_mask:0xf bank_mask:0xf
	global_store_dwordx4 v[136:137], v[130:133], off sc0 sc1 nt
	s_nop 1
	v_pk_mul_f32 v[60:61], v[40:41], v[76:77]
	v_accvgpr_read_b32 v15, a37
	v_mov_b32_e32 v2, v35
	v_mov_b32_dpp v11, v80 row_shl:1 row_mask:0xf bank_mask:0xf
	v_pk_fma_f32 v[60:61], v[80:81], v[14:15], v[60:61] op_sel_hi:[0,1,1]
	v_pk_mov_b32 v[62:63], v[80:81], v[66:67] op_sel:[1,0]
	v_mov_b32_dpp v2, v85 row_shr:1 row_mask:0xf bank_mask:0xf
	v_mov_b32_e32 v23, v85
	v_accvgpr_read_b32 v15, a9
	v_pk_fma_f32 v[60:61], v[62:63], v[10:11], v[60:61]
	v_pk_mul_f32 v[62:63], v[22:23], v[2:3]
	v_accvgpr_read_b32 v14, a8
	v_mov_b32_dpp v35, v84 row_shl:1 row_mask:0xf bank_mask:0xf
	v_pk_fma_f32 v[62:63], v[84:85], v[100:101], v[62:63] op_sel_hi:[0,1,1]
	v_pk_mov_b32 v[68:69], v[84:85], v[14:15] op_sel:[1,0]
	v_mov_b32_e32 v92, v59
	v_pk_fma_f32 v[62:63], v[68:69], v[34:35], v[62:63]
	v_pk_add_f32 v[60:61], v[60:61], 0 op_sel_hi:[1,0]
	v_mov_b32_dpp v92, v125 row_shr:1 row_mask:0xf bank_mask:0xf
	v_mov_b32_e32 v97, v125
	v_accvgpr_read_b32 v71, a15
	v_pk_add_f32 v[60:61], v[60:61], v[62:63]
	v_pk_mul_f32 v[62:63], v[96:97], v[92:93]
	v_accvgpr_read_b32 v70, a14
	v_mov_b32_dpp v59, v124 row_shl:1 row_mask:0xf bank_mask:0xf
	v_pk_fma_f32 v[62:63], v[124:125], v[16:17], v[62:63] op_sel_hi:[0,1,1]
	v_pk_mov_b32 v[68:69], v[124:125], v[70:71] op_sel:[1,0]
	v_mov_b32_e32 v94, v57
	v_pk_fma_f32 v[62:63], v[68:69], v[58:59], v[62:63]
	s_mov_b64 s[0:1], 0x820000
	v_pk_add_f32 v[60:61], v[60:61], v[62:63]
	v_mov_b32_dpp v94, v123 row_shr:1 row_mask:0xf bank_mask:0xf
	v_mov_b32_e32 v99, v123
	v_accvgpr_write_b32 a31, v17
	v_lshl_add_u64 v[62:63], v[54:55], 0, s[0:1]
	v_mov_b32_e32 v128, v60
	v_mov_b32_e32 v129, v61
	v_pk_mul_f32 v[60:61], v[98:99], v[94:95]
	v_mov_b32_e32 v102, v51
	v_accvgpr_write_b32 a30, v16
	v_mov_b32_dpp v57, v122 row_shl:1 row_mask:0xf bank_mask:0xf
	v_pk_fma_f32 v[60:61], v[122:123], v[28:29], v[60:61] op_sel_hi:[0,1,1]
	v_mov_b32_e32 v62, v123
	v_mov_b32_e32 v63, v67
	v_mov_b32_dpp v102, v121 row_shr:1 row_mask:0xf bank_mask:0xf
	v_mov_b32_e32 v105, v121
	v_accvgpr_read_b32 v16, a28
	v_pk_fma_f32 v[60:61], v[62:63], v[56:57], v[60:61]
	v_pk_mul_f32 v[62:63], v[104:105], v[102:103]
	v_accvgpr_read_b32 v17, a29
	v_mov_b32_dpp v51, v120 row_shl:1 row_mask:0xf bank_mask:0xf
	v_pk_fma_f32 v[62:63], v[120:121], v[16:17], v[62:63] op_sel_hi:[0,1,1]
	v_mov_b32_e32 v68, v121
	v_mov_b32_e32 v69, v15
	v_mov_b32_e32 v108, v49
	v_pk_fma_f32 v[62:63], v[68:69], v[50:51], v[62:63]
	v_pk_add_f32 v[60:61], v[60:61], 0 op_sel_hi:[1,0]
	v_mov_b32_dpp v108, v91 row_shr:1 row_mask:0xf bank_mask:0xf
	v_mov_b32_e32 v111, v91
	v_pk_add_f32 v[60:61], v[60:61], v[62:63]
	v_pk_mul_f32 v[62:63], v[110:111], v[108:109]
	v_mov_b32_dpp v49, v90 row_shl:1 row_mask:0xf bank_mask:0xf
	v_pk_fma_f32 v[62:63], v[90:91], v[30:31], v[62:63] op_sel_hi:[0,1,1]
	v_mov_b32_e32 v68, v91
	v_mov_b32_e32 v69, v71
	v_pk_fma_f32 v[62:63], v[68:69], v[48:49], v[62:63]
	s_mov_b64 s[0:1], 0x830000
	v_mov_b32_e32 v0, v22
	v_pk_add_f32 v[60:61], v[60:61], v[62:63]
	v_lshl_add_u64 v[136:137], v[134:135], 0, s[0:1]
	s_add_u32 s0, s10, 0x1c00000
	v_accvgpr_read_b32 v22, a50
	v_accvgpr_read_b32 v1, a72
	s_addc_u32 s1, s11, 0
	v_accvgpr_read_b32 v23, a51
	s_nop 1
	s_mov_b64 vcc, s[28:29]
	s_nop 0
	v_cndmask_b32_dpp v130, v60, v128, vcc quad_perm:[1,0,3,2] row_mask:0xf bank_mask:0xf
	v_cndmask_b32_dpp v131, v61, v129, vcc quad_perm:[1,0,3,2] row_mask:0xf bank_mask:0xf
	s_mov_b64 vcc, s[30:31]
	s_nop 0
	v_cndmask_b32_dpp v132, v128, v60, vcc quad_perm:[1,0,3,2] row_mask:0xf bank_mask:0xf
	v_cndmask_b32_dpp v133, v129, v61, vcc quad_perm:[1,0,3,2] row_mask:0xf bank_mask:0xf
	global_store_dwordx4 v[136:137], v[130:133], off sc0 sc1 nt
	s_nop 1
	v_readfirstlane_b32 s2, v1
	v_lshl_add_u64 v[60:61], s[0:1], 0, v[22:23]
	v_accvgpr_read_b32 v1, a12
	v_accvgpr_read_b32 v22, a52
	s_waitcnt vmcnt(18)
	s_mov_b32 m0, s2
	v_readfirstlane_b32 s2, v1
	v_accvgpr_read_b32 v23, a53
	v_accvgpr_read_b32 v1, a13
	s_waitcnt lgkmcnt(0)
	s_barrier
	global_load_lds_dwordx4 v[60:61], off nt
	v_lshl_add_u64 v[60:61], s[0:1], 0, v[22:23]
	s_mov_b32 m0, s2
	v_readfirstlane_b32 s2, v1
	v_accvgpr_read_b32 v1, a16
	global_load_lds_dwordx4 v[60:61], off nt
	v_lshl_add_u64 v[60:61], s[0:1], 0, v[114:115]
	s_mov_b32 m0, s2
	v_readfirstlane_b32 s2, v1
	global_load_lds_dwordx4 v[60:61], off nt
	v_lshl_add_u64 v[60:61], s[0:1], 0, v[116:117]
	s_mov_b32 m0, s2
	v_accvgpr_write_b32 a22, v30
	v_accvgpr_write_b32 a44, v70
	global_load_lds_dwordx4 v[60:61], off nt
	v_accvgpr_write_b32 a2, v106
	v_accvgpr_write_b32 a34, v74
	v_accvgpr_write_b32 a23, v31
	v_accvgpr_write_b32 a45, v71
	v_add_u32_e32 v2, 0x7010, v5
	v_mov_b32_e32 v31, v5
	v_add_u32_e32 v5, 0x7000, v4
	ds_read_b64 v[60:61], v2
	ds_read_b64 v[62:63], v2 offset:288
	ds_read_b64 v[68:69], v2 offset:576
	ds_read_b64 v[70:71], v2 offset:1728
	ds_read_b64 v[72:73], v2 offset:2016
	ds_read_b64 v[82:83], v2 offset:2304
	ds_read_b64 v[80:81], v2 offset:3456
	ds_read_b64 v[84:85], v2 offset:3744
	ds_read_b64 v[116:117], v2 offset:4032
	ds_read_b64 v[114:115], v2 offset:5184
	ds_read_b64 v[112:113], v2 offset:5472
	ds_read_b64 v[90:91], v2 offset:5760
	ds_read_b32 v43, v5
	ds_read_b32 v19, v5 offset:288
	ds_read_b32 v39, v5 offset:576
	ds_read_b32 v25, v5 offset:1728
	ds_read_b32 v7, v5 offset:2016
	ds_read_b32 v21, v5 offset:2304
	ds_read_b32 v11, v5 offset:3456
	ds_read_b32 v35, v5 offset:3744
	ds_read_b32 v59, v5 offset:4032
	ds_read_b32 v57, v5 offset:5184
	ds_read_b32 v51, v5 offset:5472
	ds_read_b32 v49, v5 offset:5760
	s_waitcnt lgkmcnt(0)
	v_accvgpr_write_b32 a3, v107
	v_mov_b32_e32 v46, v43
	v_accvgpr_write_b32 a35, v75
	v_accvgpr_read_b32 v74, a40
	v_mov_b32_dpp v46, v61 row_shr:1 row_mask:0xf bank_mask:0xf
	v_mov_b32_e32 v75, v61
	v_accvgpr_read_b32 v107, a39
	v_accvgpr_write_b32 a10, v100
	v_pk_mul_f32 v[86:87], v[74:75], v[46:47]
	v_accvgpr_read_b32 v106, a38
	v_mov_b32_e32 v26, v19
	v_accvgpr_write_b32 a11, v101
	v_mov_b32_dpp v43, v60 row_shl:1 row_mask:0xf bank_mask:0xf
	v_mov_b32_e32 v32, v74
	v_pk_fma_f32 v[86:87], v[60:61], v[8:9], v[86:87] op_sel_hi:[0,1,1]
	v_pk_mov_b32 v[60:61], v[60:61], v[106:107] op_sel:[1,0]
	v_mov_b32_dpp v26, v63 row_shr:1 row_mask:0xf bank_mask:0xf
	v_accvgpr_read_b32 v74, a24
	v_mov_b32_e32 v75, v63
	v_accvgpr_read_b32 v101, a35
	v_pk_fma_f32 v[60:61], v[60:61], v[42:43], v[86:87]
	v_pk_mul_f32 v[86:87], v[74:75], v[26:27]
	v_accvgpr_read_b32 v100, a34
	v_accvgpr_write_b32 a14, v66
	v_mov_b32_dpp v19, v62 row_shl:1 row_mask:0xf bank_mask:0xf
	v_pk_fma_f32 v[86:87], v[62:63], v[126:127], v[86:87] op_sel_hi:[0,1,1]
	v_pk_mov_b32 v[62:63], v[62:63], v[100:101] op_sel:[1,0]
	v_mov_b32_e32 v44, v39
	v_accvgpr_write_b32 a42, v64
	v_accvgpr_write_b32 a15, v67
	v_mov_b32_e32 v66, v4
	v_pk_fma_f32 v[62:63], v[62:63], v[18:19], v[86:87]
	v_pk_add_f32 v[60:61], v[60:61], 0 op_sel_hi:[1,0]
	v_mov_b32_dpp v44, v69 row_shr:1 row_mask:0xf bank_mask:0xf
	v_accvgpr_read_b32 v64, a48
	v_mov_b32_e32 v65, v69
	v_accvgpr_read_b32 v4, a46
	v_pk_add_f32 v[60:61], v[60:61], v[62:63]
	v_pk_mul_f32 v[62:63], v[64:65], v[44:45]
	v_accvgpr_read_b32 v5, a47
	v_mov_b32_dpp v39, v68 row_shl:1 row_mask:0xf bank_mask:0xf
	v_pk_fma_f32 v[62:63], v[68:69], v[88:89], v[62:63] op_sel_hi:[0,1,1]
	v_pk_mov_b32 v[68:69], v[68:69], v[4:5] op_sel:[1,0]
	v_mov_b32_e32 v36, v25
	v_pk_fma_f32 v[62:63], v[68:69], v[38:39], v[62:63]
	s_mov_b64 s[0:1], 0xc00000
	v_pk_add_f32 v[60:61], v[60:61], v[62:63]
	v_mov_b32_dpp v36, v71 row_shr:1 row_mask:0xf bank_mask:0xf
	v_accvgpr_read_b32 v22, a42
	v_mov_b32_e32 v23, v71
	v_accvgpr_mov_b32 a26, a20
	v_accvgpr_write_b32 a20, v28
	v_lshl_add_u64 v[62:63], v[54:55], 0, s[0:1]
	v_mov_b32_e32 v128, v60
	v_mov_b32_e32 v129, v61
	v_pk_mul_f32 v[60:61], v[22:23], v[36:37]
	v_mov_b32_e32 v12, v7
	v_accvgpr_write_b32 a21, v29
	v_mov_b32_dpp v25, v70 row_shl:1 row_mask:0xf bank_mask:0xf
	v_pk_fma_f32 v[60:61], v[70:71], v[118:119], v[60:61] op_sel_hi:[0,1,1]
	v_mov_b32_e32 v62, v71
	v_mov_b32_e32 v63, v107
	v_mov_b32_dpp v12, v73 row_shr:1 row_mask:0xf bank_mask:0xf
	v_accvgpr_read_b32 v28, a26
	v_mov_b32_e32 v29, v73
	v_accvgpr_read_b32 v121, a3
	v_pk_fma_f32 v[60:61], v[62:63], v[24:25], v[60:61]
	v_pk_mul_f32 v[62:63], v[28:29], v[12:13]
	v_accvgpr_read_b32 v120, a2
	v_mov_b32_dpp v7, v72 row_shl:1 row_mask:0xf bank_mask:0xf
	v_pk_fma_f32 v[62:63], v[72:73], v[120:121], v[62:63] op_sel_hi:[0,1,1]
	v_mov_b32_e32 v68, v73
	v_mov_b32_e32 v69, v101
	v_mov_b32_e32 v78, v21
	v_pk_fma_f32 v[62:63], v[68:69], v[6:7], v[62:63]
	v_pk_add_f32 v[60:61], v[60:61], 0 op_sel_hi:[1,0]
	v_mov_b32_dpp v78, v83 row_shr:1 row_mask:0xf bank_mask:0xf
	v_mov_b32_e32 v53, v83
	v_accvgpr_read_b32 v125, a19
	v_pk_add_f32 v[60:61], v[60:61], v[62:63]
	v_pk_mul_f32 v[62:63], v[52:53], v[78:79]
	v_accvgpr_read_b32 v124, a18
	v_mov_b32_dpp v21, v82 row_shl:1 row_mask:0xf bank_mask:0xf
	v_pk_fma_f32 v[62:63], v[82:83], v[124:125], v[62:63] op_sel_hi:[0,1,1]
	v_mov_b32_e32 v68, v83
	v_mov_b32_e32 v69, v5
	v_pk_fma_f32 v[62:63], v[68:69], v[20:21], v[62:63]
	v_mov_b32_e32 v76, v11
	v_pk_add_f32 v[60:61], v[60:61], v[62:63]
	s_mov_b64 s[0:1], 0xc10000
	v_mov_b32_dpp v76, v81 row_shr:1 row_mask:0xf bank_mask:0xf
	v_mov_b32_e32 v41, v81
	v_accvgpr_read_b32 v123, a37
	v_accvgpr_read_b32 v4, a14
	v_lshl_add_u64 v[136:137], v[134:135], 0, s[0:1]
	s_nop 1
	s_mov_b64 vcc, s[28:29]
	s_nop 0
	v_cndmask_b32_dpp v130, v60, v128, vcc quad_perm:[1,0,3,2] row_mask:0xf bank_mask:0xf
	v_cndmask_b32_dpp v131, v61, v129, vcc quad_perm:[1,0,3,2] row_mask:0xf bank_mask:0xf
	s_mov_b64 vcc, s[30:31]
	s_nop 0
	v_cndmask_b32_dpp v132, v128, v60, vcc quad_perm:[1,0,3,2] row_mask:0xf bank_mask:0xf
	v_cndmask_b32_dpp v133, v129, v61, vcc quad_perm:[1,0,3,2] row_mask:0xf bank_mask:0xf
	global_store_dwordx4 v[136:137], v[130:133], off sc0 sc1 nt
	s_nop 1
	v_pk_mul_f32 v[60:61], v[40:41], v[76:77]
	v_accvgpr_read_b32 v122, a36
	v_accvgpr_read_b32 v5, a15
	v_mov_b32_e32 v2, v35
	v_accvgpr_mov_b32 a32, a24
	v_accvgpr_write_b32 a24, v22
	v_mov_b64_e32 v[22:23], v[118:119]
	v_mov_b32_dpp v11, v80 row_shl:1 row_mask:0xf bank_mask:0xf
	v_pk_fma_f32 v[60:61], v[80:81], v[122:123], v[60:61] op_sel_hi:[0,1,1]
	v_pk_mov_b32 v[62:63], v[80:81], v[4:5] op_sel:[1,0]
	v_mov_b32_dpp v2, v85 row_shr:1 row_mask:0xf bank_mask:0xf
	v_mov_b32_e32 v106, v0
	v_mov_b32_e32 v107, v85
	v_accvgpr_read_b32 v119, a11
	v_pk_fma_f32 v[60:61], v[62:63], v[10:11], v[60:61]
	v_pk_mul_f32 v[62:63], v[106:107], v[2:3]
	v_accvgpr_read_b32 v118, a10
	v_mov_b64_e32 v[100:101], v[14:15]
	v_mov_b32_dpp v35, v84 row_shl:1 row_mask:0xf bank_mask:0xf
	v_pk_fma_f32 v[62:63], v[84:85], v[118:119], v[62:63] op_sel_hi:[0,1,1]
	v_pk_mov_b32 v[68:69], v[84:85], v[100:101] op_sel:[1,0]
	v_mov_b32_e32 v92, v59
	v_accvgpr_write_b32 a26, v52
	v_mov_b32_e32 v74, v40
	v_pk_fma_f32 v[62:63], v[68:69], v[34:35], v[62:63]
	v_pk_add_f32 v[60:61], v[60:61], 0 op_sel_hi:[1,0]
	v_mov_b32_dpp v92, v117 row_shr:1 row_mask:0xf bank_mask:0xf
	v_mov_b32_e32 v97, v117
	v_accvgpr_read_b32 v41, a31
	v_accvgpr_read_b32 v53, a45
	v_pk_add_f32 v[60:61], v[60:61], v[62:63]
	v_pk_mul_f32 v[62:63], v[96:97], v[92:93]
	v_accvgpr_read_b32 v40, a30
	v_accvgpr_read_b32 v52, a44
	v_mov_b32_dpp v59, v116 row_shl:1 row_mask:0xf bank_mask:0xf
	v_pk_fma_f32 v[62:63], v[116:117], v[40:41], v[62:63] op_sel_hi:[0,1,1]
	v_pk_mov_b32 v[68:69], v[116:117], v[52:53] op_sel:[1,0]
	v_mov_b32_e32 v94, v57
	v_pk_fma_f32 v[62:63], v[68:69], v[58:59], v[62:63]
	s_mov_b64 s[0:1], 0xc20000
	v_pk_add_f32 v[60:61], v[60:61], v[62:63]
	v_mov_b32_dpp v94, v115 row_shr:1 row_mask:0xf bank_mask:0xf
	v_mov_b32_e32 v99, v115
	v_accvgpr_read_b32 v14, a20
	v_lshl_add_u64 v[62:63], v[54:55], 0, s[0:1]
	v_mov_b32_e32 v128, v60
	v_mov_b32_e32 v129, v61
	v_pk_mul_f32 v[60:61], v[98:99], v[94:95]
	v_accvgpr_read_b32 v15, a21
	v_mov_b32_e32 v102, v51
	v_mov_b32_dpp v57, v114 row_shl:1 row_mask:0xf bank_mask:0xf
	v_pk_fma_f32 v[60:61], v[114:115], v[14:15], v[60:61] op_sel_hi:[0,1,1]
	v_mov_b32_e32 v62, v115
	v_mov_b32_e32 v63, v5
	v_mov_b32_dpp v102, v113 row_shr:1 row_mask:0xf bank_mask:0xf
	v_mov_b32_e32 v105, v113
	v_pk_fma_f32 v[60:61], v[62:63], v[56:57], v[60:61]
	v_pk_mul_f32 v[62:63], v[104:105], v[102:103]
	v_accvgpr_write_b32 a8, v8
	v_mov_b32_dpp v51, v112 row_shl:1 row_mask:0xf bank_mask:0xf
	v_pk_fma_f32 v[62:63], v[112:113], v[16:17], v[62:63] op_sel_hi:[0,1,1]
	v_mov_b32_e32 v68, v113
	v_mov_b32_e32 v69, v101
	v_mov_b32_e32 v108, v49
	v_accvgpr_write_b32 a9, v9
	v_pk_fma_f32 v[62:63], v[68:69], v[50:51], v[62:63]
	v_pk_add_f32 v[60:61], v[60:61], 0 op_sel_hi:[1,0]
	v_mov_b32_dpp v108, v91 row_shr:1 row_mask:0xf bank_mask:0xf
	v_mov_b32_e32 v111, v91
	v_accvgpr_read_b32 v8, a22
	v_pk_add_f32 v[60:61], v[60:61], v[62:63]
	v_pk_mul_f32 v[62:63], v[110:111], v[108:109]
	v_accvgpr_read_b32 v9, a23
	v_mov_b32_dpp v49, v90 row_shl:1 row_mask:0xf bank_mask:0xf
	v_pk_fma_f32 v[62:63], v[90:91], v[8:9], v[62:63] op_sel_hi:[0,1,1]
	v_mov_b32_e32 v68, v91
	v_mov_b32_e32 v69, v53
	v_pk_fma_f32 v[62:63], v[68:69], v[48:49], v[62:63]
	s_mov_b64 s[0:1], 0xc30000
	v_pk_add_f32 v[60:61], v[60:61], v[62:63]
	v_lshl_add_u64 v[136:137], v[134:135], 0, s[0:1]
	s_nop 1
	s_mov_b64 vcc, s[28:29]
	s_nop 0
	v_cndmask_b32_dpp v130, v60, v128, vcc quad_perm:[1,0,3,2] row_mask:0xf bank_mask:0xf
	v_cndmask_b32_dpp v131, v61, v129, vcc quad_perm:[1,0,3,2] row_mask:0xf bank_mask:0xf
	s_mov_b64 vcc, s[30:31]
	s_nop 0
	v_cndmask_b32_dpp v132, v128, v60, vcc quad_perm:[1,0,3,2] row_mask:0xf bank_mask:0xf
	v_cndmask_b32_dpp v133, v129, v61, vcc quad_perm:[1,0,3,2] row_mask:0xf bank_mask:0xf
	global_store_dwordx4 v[136:137], v[130:133], off sc0 sc1 nt
	s_nop 1
	s_waitcnt vmcnt(20)
	v_accvgpr_write_b32 a16, v88
	v_accvgpr_write_b32 a10, v100
	s_waitcnt lgkmcnt(0)
	s_barrier
	v_add_u32_e32 v2, 0xe010, v31
	v_add_u32_e32 v5, 0xe000, v66
	ds_read_b64 v[60:61], v2
	ds_read_b64 v[62:63], v2 offset:288
	ds_read_b64 v[68:69], v2 offset:576
	ds_read_b64 v[70:71], v2 offset:1728
	ds_read_b64 v[72:73], v2 offset:2016
	ds_read_b64 v[82:83], v2 offset:2304
	ds_read_b64 v[80:81], v2 offset:3456
	ds_read_b64 v[84:85], v2 offset:3744
	ds_read_b64 v[116:117], v2 offset:4032
	ds_read_b64 v[114:115], v2 offset:5184
	ds_read_b64 v[112:113], v2 offset:5472
	ds_read_b64 v[90:91], v2 offset:5760
	ds_read_b32 v43, v5
	ds_read_b32 v19, v5 offset:288
	ds_read_b32 v39, v5 offset:576
	ds_read_b32 v25, v5 offset:1728
	ds_read_b32 v7, v5 offset:2016
	ds_read_b32 v21, v5 offset:2304
	ds_read_b32 v11, v5 offset:3456
	ds_read_b32 v35, v5 offset:3744
	ds_read_b32 v59, v5 offset:4032
	ds_read_b32 v57, v5 offset:5184
	ds_read_b32 v51, v5 offset:5472
	ds_read_b32 v49, v5 offset:5760
	s_waitcnt lgkmcnt(0)
	v_accvgpr_write_b32 a17, v89
	v_mov_b32_e32 v46, v43
	v_accvgpr_write_b32 a11, v101
	v_mov_b32_e32 v33, v61
	v_mov_b32_dpp v46, v61 row_shr:1 row_mask:0xf bank_mask:0xf
	v_accvgpr_read_b32 v89, a9
	v_accvgpr_read_b32 v101, a39
	v_pk_mul_f32 v[86:87], v[32:33], v[46:47]
	v_accvgpr_read_b32 v88, a8
	v_accvgpr_read_b32 v100, a38
	v_mov_b32_e32 v26, v19
	v_accvgpr_write_b32 a19, v17
	v_mov_b32_dpp v43, v60 row_shl:1 row_mask:0xf bank_mask:0xf
	v_pk_fma_f32 v[86:87], v[60:61], v[88:89], v[86:87] op_sel_hi:[0,1,1]
	v_pk_mov_b32 v[60:61], v[60:61], v[100:101] op_sel:[1,0]
	v_mov_b32_dpp v26, v63 row_shr:1 row_mask:0xf bank_mask:0xf
	v_accvgpr_read_b32 v0, a32
	v_mov_b32_e32 v1, v63
	v_accvgpr_read_b32 v4, a34
	v_accvgpr_write_b32 a18, v16
	v_pk_fma_f32 v[60:61], v[60:61], v[42:43], v[86:87]
	v_pk_mul_f32 v[86:87], v[0:1], v[26:27]
	v_mov_b64_e32 v[16:17], v[126:127]
	v_accvgpr_read_b32 v5, a35
	v_mov_b32_dpp v19, v62 row_shl:1 row_mask:0xf bank_mask:0xf
	v_pk_fma_f32 v[86:87], v[62:63], v[16:17], v[86:87] op_sel_hi:[0,1,1]
	v_pk_mov_b32 v[62:63], v[62:63], v[4:5] op_sel:[1,0]
	v_mov_b32_e32 v44, v39
	v_accvgpr_read_b32 v30, a48
	v_mov_b32_e32 v64, v28
	v_accvgpr_write_b32 a7, v66
	v_pk_fma_f32 v[62:63], v[62:63], v[18:19], v[86:87]
	v_pk_add_f32 v[60:61], v[60:61], 0 op_sel_hi:[1,0]
	v_mov_b32_dpp v44, v69 row_shr:1 row_mask:0xf bank_mask:0xf
	v_mov_b32_e32 v31, v69
	v_accvgpr_read_b32 v29, a17
	v_accvgpr_read_b32 v67, a47
	v_pk_add_f32 v[60:61], v[60:61], v[62:63]
	v_pk_mul_f32 v[62:63], v[30:31], v[44:45]
	v_accvgpr_read_b32 v28, a16
	v_accvgpr_read_b32 v66, a46
	v_mov_b32_dpp v39, v68 row_shl:1 row_mask:0xf bank_mask:0xf
	v_pk_fma_f32 v[62:63], v[68:69], v[28:29], v[62:63] op_sel_hi:[0,1,1]
	v_pk_mov_b32 v[68:69], v[68:69], v[66:67] op_sel:[1,0]
	v_mov_b32_e32 v36, v25
	v_pk_fma_f32 v[62:63], v[68:69], v[38:39], v[62:63]
	s_mov_b64 s[0:1], 0x1000000
	v_pk_add_f32 v[60:61], v[60:61], v[62:63]
	v_mov_b32_dpp v36, v71 row_shr:1 row_mask:0xf bank_mask:0xf
	v_accvgpr_read_b32 v126, a24
	v_mov_b32_e32 v127, v71
	v_lshl_add_u64 v[62:63], v[54:55], 0, s[0:1]
	v_mov_b32_e32 v128, v60
	v_mov_b32_e32 v129, v61
	v_pk_mul_f32 v[60:61], v[126:127], v[36:37]
	v_mov_b32_e32 v12, v7
	v_mov_b32_dpp v25, v70 row_shl:1 row_mask:0xf bank_mask:0xf
	v_pk_fma_f32 v[60:61], v[70:71], v[22:23], v[60:61] op_sel_hi:[0,1,1]
	v_mov_b32_e32 v62, v71
	v_mov_b32_e32 v63, v101
	v_mov_b32_dpp v12, v73 row_shr:1 row_mask:0xf bank_mask:0xf
	v_mov_b32_e32 v52, v64
	v_mov_b32_e32 v53, v73
	v_pk_fma_f32 v[60:61], v[62:63], v[24:25], v[60:61]
	v_pk_mul_f32 v[62:63], v[52:53], v[12:13]
	v_mov_b32_dpp v7, v72 row_shl:1 row_mask:0xf bank_mask:0xf
	v_pk_fma_f32 v[62:63], v[72:73], v[120:121], v[62:63] op_sel_hi:[0,1,1]
	v_mov_b32_e32 v68, v73
	v_mov_b32_e32 v69, v5
	v_mov_b32_e32 v78, v21
	v_pk_fma_f32 v[62:63], v[68:69], v[6:7], v[62:63]
	v_pk_add_f32 v[60:61], v[60:61], 0 op_sel_hi:[1,0]
	v_mov_b32_dpp v78, v83 row_shr:1 row_mask:0xf bank_mask:0xf
	v_accvgpr_read_b32 v4, a26
	v_mov_b32_e32 v5, v83
	v_pk_add_f32 v[60:61], v[60:61], v[62:63]
	v_pk_mul_f32 v[62:63], v[4:5], v[78:79]
	v_mov_b32_dpp v21, v82 row_shl:1 row_mask:0xf bank_mask:0xf
	v_pk_fma_f32 v[62:63], v[82:83], v[124:125], v[62:63] op_sel_hi:[0,1,1]
	v_mov_b32_e32 v68, v83
	v_mov_b32_e32 v69, v67
	v_accvgpr_write_b32 a8, v120
	v_pk_fma_f32 v[62:63], v[68:69], v[20:21], v[62:63]
	v_mov_b32_e32 v76, v11
	v_accvgpr_write_b32 a9, v121
	v_pk_add_f32 v[60:61], v[60:61], v[62:63]
	s_mov_b64 s[0:1], 0x1010000
	v_mov_b32_dpp v76, v81 row_shr:1 row_mask:0xf bank_mask:0xf
	v_mov_b32_e32 v120, v74
	v_mov_b32_e32 v121, v81
	v_accvgpr_read_b32 v101, a15
	v_accvgpr_mov_b32 a12, a38
	v_lshl_add_u64 v[136:137], v[134:135], 0, s[0:1]
	s_nop 1
	s_mov_b64 vcc, s[28:29]
	s_nop 0
	v_cndmask_b32_dpp v130, v60, v128, vcc quad_perm:[1,0,3,2] row_mask:0xf bank_mask:0xf
	v_cndmask_b32_dpp v131, v61, v129, vcc quad_perm:[1,0,3,2] row_mask:0xf bank_mask:0xf
	s_mov_b64 vcc, s[30:31]
	s_nop 0
	v_cndmask_b32_dpp v132, v128, v60, vcc quad_perm:[1,0,3,2] row_mask:0xf bank_mask:0xf
	v_cndmask_b32_dpp v133, v129, v61, vcc quad_perm:[1,0,3,2] row_mask:0xf bank_mask:0xf
	global_store_dwordx4 v[136:137], v[130:133], off sc0 sc1 nt
	s_nop 1
	v_pk_mul_f32 v[60:61], v[120:121], v[76:77]
	v_accvgpr_read_b32 v100, a14
	v_mov_b32_e32 v2, v35
	v_accvgpr_mov_b32 a13, a39
	v_accvgpr_write_b32 a20, v22
	v_mov_b32_dpp v11, v80 row_shl:1 row_mask:0xf bank_mask:0xf
	v_pk_fma_f32 v[60:61], v[80:81], v[122:123], v[60:61] op_sel_hi:[0,1,1]
	v_pk_mov_b32 v[62:63], v[80:81], v[100:101] op_sel:[1,0]
	v_mov_b32_dpp v2, v85 row_shr:1 row_mask:0xf bank_mask:0xf
	v_mov_b32_e32 v107, v85
	v_accvgpr_read_b32 v123, a11
	v_accvgpr_write_b32 a21, v23
	v_accvgpr_read_b32 v23, a13
	v_pk_fma_f32 v[60:61], v[62:63], v[10:11], v[60:61]
	v_pk_mul_f32 v[62:63], v[106:107], v[2:3]
	v_accvgpr_read_b32 v122, a10
	v_accvgpr_read_b32 v22, a12
	v_mov_b32_dpp v35, v84 row_shl:1 row_mask:0xf bank_mask:0xf
	v_pk_fma_f32 v[62:63], v[84:85], v[118:119], v[62:63] op_sel_hi:[0,1,1]
	v_accvgpr_write_b32 a12, v118
	v_pk_mov_b32 v[68:69], v[84:85], v[122:123] op_sel:[1,0]
	v_mov_b32_e32 v92, v59
	v_accvgpr_write_b32 a13, v119
	v_pk_fma_f32 v[62:63], v[68:69], v[34:35], v[62:63]
	v_pk_add_f32 v[60:61], v[60:61], 0 op_sel_hi:[1,0]
	v_mov_b32_dpp v92, v117 row_shr:1 row_mask:0xf bank_mask:0xf
	v_mov_b32_e32 v97, v117
	v_mov_b64_e32 v[118:119], v[40:41]
	v_accvgpr_read_b32 v40, a44
	v_pk_add_f32 v[60:61], v[60:61], v[62:63]
	v_pk_mul_f32 v[62:63], v[96:97], v[92:93]
	v_accvgpr_read_b32 v41, a45
	v_mov_b32_dpp v59, v116 row_shl:1 row_mask:0xf bank_mask:0xf
	v_pk_fma_f32 v[62:63], v[116:117], v[118:119], v[62:63] op_sel_hi:[0,1,1]
	v_pk_mov_b32 v[68:69], v[116:117], v[40:41] op_sel:[1,0]
	v_mov_b32_e32 v94, v57
	v_pk_fma_f32 v[62:63], v[68:69], v[58:59], v[62:63]
	s_mov_b64 s[0:1], 0x1020000
	v_pk_add_f32 v[60:61], v[60:61], v[62:63]
	v_mov_b32_dpp v94, v115 row_shr:1 row_mask:0xf bank_mask:0xf
	v_mov_b32_e32 v99, v115
	v_lshl_add_u64 v[62:63], v[54:55], 0, s[0:1]
	v_mov_b32_e32 v128, v60
	v_mov_b32_e32 v129, v61
	v_pk_mul_f32 v[60:61], v[98:99], v[94:95]
	v_mov_b32_e32 v102, v51
	v_accvgpr_write_b32 a30, v4
	v_mov_b32_dpp v57, v114 row_shl:1 row_mask:0xf bank_mask:0xf
	v_pk_fma_f32 v[60:61], v[114:115], v[14:15], v[60:61] op_sel_hi:[0,1,1]
	v_mov_b32_e32 v62, v115
	v_mov_b32_e32 v63, v101
	v_mov_b32_dpp v102, v113 row_shr:1 row_mask:0xf bank_mask:0xf
	v_mov_b32_e32 v105, v113
	v_accvgpr_read_b32 v4, a18
	v_pk_fma_f32 v[60:61], v[62:63], v[56:57], v[60:61]
	v_pk_mul_f32 v[62:63], v[104:105], v[102:103]
	v_accvgpr_read_b32 v5, a19
	v_mov_b32_dpp v51, v112 row_shl:1 row_mask:0xf bank_mask:0xf
	v_pk_fma_f32 v[62:63], v[112:113], v[4:5], v[62:63] op_sel_hi:[0,1,1]
	v_mov_b32_e32 v68, v113
	v_mov_b32_e32 v69, v123
	v_mov_b32_e32 v108, v49
	v_pk_fma_f32 v[62:63], v[68:69], v[50:51], v[62:63]
	v_pk_add_f32 v[60:61], v[60:61], 0 op_sel_hi:[1,0]
	v_mov_b32_dpp v108, v91 row_shr:1 row_mask:0xf bank_mask:0xf
	v_mov_b32_e32 v111, v91
	v_pk_add_f32 v[60:61], v[60:61], v[62:63]
	v_pk_mul_f32 v[62:63], v[110:111], v[108:109]
	v_mov_b32_dpp v49, v90 row_shl:1 row_mask:0xf bank_mask:0xf
	v_pk_fma_f32 v[62:63], v[90:91], v[8:9], v[62:63] op_sel_hi:[0,1,1]
	v_mov_b32_e32 v68, v91
	v_mov_b32_e32 v69, v41
	v_pk_fma_f32 v[62:63], v[68:69], v[48:49], v[62:63]
	s_mov_b64 s[0:1], 0x1030000
	v_pk_add_f32 v[60:61], v[60:61], v[62:63]
	v_lshl_add_u64 v[136:137], v[134:135], 0, s[0:1]
	s_nop 1
	s_mov_b64 vcc, s[28:29]
	s_nop 0
	v_cndmask_b32_dpp v130, v60, v128, vcc quad_perm:[1,0,3,2] row_mask:0xf bank_mask:0xf
	v_cndmask_b32_dpp v131, v61, v129, vcc quad_perm:[1,0,3,2] row_mask:0xf bank_mask:0xf
	s_mov_b64 vcc, s[30:31]
	s_nop 0
	v_cndmask_b32_dpp v132, v128, v60, vcc quad_perm:[1,0,3,2] row_mask:0xf bank_mask:0xf
	v_cndmask_b32_dpp v133, v129, v61, vcc quad_perm:[1,0,3,2] row_mask:0xf bank_mask:0xf
	global_store_dwordx4 v[136:137], v[130:133], off sc0 sc1 nt
	s_nop 1
	s_waitcnt vmcnt(16)
	s_waitcnt lgkmcnt(0)
	s_barrier
	v_accvgpr_read_b32 v2, a0
	v_accvgpr_read_b32 v8, a4
	ds_read_b64 v[60:61], v8
	ds_read_b64 v[62:63], v8 offset:288
	ds_read_b64 v[68:69], v8 offset:576
	ds_read_b64 v[70:71], v8 offset:1728
	ds_read_b64 v[72:73], v8 offset:2016
	ds_read_b64 v[82:83], v8 offset:2304
	ds_read_b64 v[80:81], v8 offset:3456
	ds_read_b64 v[84:85], v8 offset:3744
	ds_read_b64 v[116:117], v8 offset:4032
	ds_read_b64 v[114:115], v8 offset:5184
	ds_read_b64 v[112:113], v8 offset:5472
	ds_read_b64 v[90:91], v8 offset:5760
	ds_read_b32 v43, v2
	ds_read_b32 v19, v2 offset:288
	ds_read_b32 v39, v2 offset:576
	ds_read_b32 v25, v2 offset:1728
	ds_read_b32 v7, v2 offset:2016
	ds_read_b32 v21, v2 offset:2304
	ds_read_b32 v11, v2 offset:3456
	ds_read_b32 v35, v2 offset:3744
	ds_read_b32 v59, v2 offset:4032
	ds_read_b32 v57, v2 offset:5184
	ds_read_b32 v51, v2 offset:5472
	ds_read_b32 v49, v2 offset:5760
	s_waitcnt lgkmcnt(0)
	v_mov_b32_e32 v64, v32
	v_mov_b32_e32 v46, v43
	v_mov_b32_e32 v65, v61
	v_mov_b64_e32 v[100:101], v[22:23]
	v_mov_b32_dpp v46, v61 row_shr:1 row_mask:0xf bank_mask:0xf
	v_pk_mul_f32 v[86:87], v[64:65], v[46:47]
	v_mov_b32_e32 v26, v19
	v_mov_b32_dpp v43, v60 row_shl:1 row_mask:0xf bank_mask:0xf
	v_pk_fma_f32 v[86:87], v[60:61], v[88:89], v[86:87] op_sel_hi:[0,1,1]
	v_pk_mov_b32 v[60:61], v[60:61], v[100:101] op_sel:[1,0]
	v_mov_b32_dpp v26, v63 row_shr:1 row_mask:0xf bank_mask:0xf
	v_mov_b32_e32 v1, v63
	v_accvgpr_read_b32 v67, a35
	v_pk_fma_f32 v[60:61], v[60:61], v[42:43], v[86:87]
	v_pk_mul_f32 v[86:87], v[0:1], v[26:27]
	v_accvgpr_read_b32 v66, a34
	v_accvgpr_write_b32 a10, v14
	v_mov_b32_dpp v19, v62 row_shl:1 row_mask:0xf bank_mask:0xf
	v_pk_fma_f32 v[86:87], v[62:63], v[16:17], v[86:87] op_sel_hi:[0,1,1]
	v_pk_mov_b32 v[62:63], v[62:63], v[66:67] op_sel:[1,0]
	v_mov_b32_e32 v44, v39
	v_accvgpr_write_b32 a11, v15
	v_pk_fma_f32 v[62:63], v[62:63], v[18:19], v[86:87]
	v_pk_add_f32 v[60:61], v[60:61], 0 op_sel_hi:[1,0]
	v_mov_b32_dpp v44, v69 row_shr:1 row_mask:0xf bank_mask:0xf
	v_mov_b32_e32 v31, v69
	v_accvgpr_read_b32 v14, a16
	v_accvgpr_read_b32 v28, a46
	v_pk_add_f32 v[60:61], v[60:61], v[62:63]
	v_pk_mul_f32 v[62:63], v[30:31], v[44:45]
	v_accvgpr_read_b32 v15, a17
	v_accvgpr_read_b32 v29, a47
	v_mov_b32_dpp v39, v68 row_shl:1 row_mask:0xf bank_mask:0xf
	v_pk_fma_f32 v[62:63], v[68:69], v[14:15], v[62:63] op_sel_hi:[0,1,1]
	v_pk_mov_b32 v[68:69], v[68:69], v[28:29] op_sel:[1,0]
	v_mov_b32_e32 v36, v25
	v_pk_fma_f32 v[62:63], v[68:69], v[38:39], v[62:63]
	s_mov_b64 s[0:1], 0x1400000
	v_pk_add_f32 v[60:61], v[60:61], v[62:63]
	v_mov_b32_dpp v36, v71 row_shr:1 row_mask:0xf bank_mask:0xf
	v_mov_b32_e32 v127, v71
	v_accvgpr_read_b32 v8, a20
	v_lshl_add_u64 v[62:63], v[54:55], 0, s[0:1]
	v_mov_b32_e32 v128, v60
	v_mov_b32_e32 v129, v61
	v_pk_mul_f32 v[60:61], v[126:127], v[36:37]
	v_accvgpr_read_b32 v9, a21
	v_accvgpr_write_b32 a25, v23
	v_mov_b32_e32 v12, v7
	v_mov_b32_dpp v25, v70 row_shl:1 row_mask:0xf bank_mask:0xf
	v_pk_fma_f32 v[60:61], v[70:71], v[8:9], v[60:61] op_sel_hi:[0,1,1]
	v_mov_b32_e32 v62, v71
	v_mov_b32_e32 v63, v101
	v_accvgpr_write_b32 a24, v22
	v_mov_b32_dpp v12, v73 row_shr:1 row_mask:0xf bank_mask:0xf
	v_mov_b32_e32 v74, v52
	v_mov_b32_e32 v75, v73
	v_accvgpr_read_b32 v23, a9
	v_accvgpr_write_b32 a26, v124
	v_accvgpr_mov_b32 a2, a22
	v_pk_fma_f32 v[60:61], v[62:63], v[24:25], v[60:61]
	v_pk_mul_f32 v[62:63], v[74:75], v[12:13]
	v_accvgpr_read_b32 v22, a8
	v_accvgpr_write_b32 a27, v125
	v_accvgpr_mov_b32 a3, a23
	v_accvgpr_write_b32 a22, v88
	v_mov_b32_dpp v7, v72 row_shl:1 row_mask:0xf bank_mask:0xf
	v_pk_fma_f32 v[62:63], v[72:73], v[22:23], v[62:63] op_sel_hi:[0,1,1]
	v_mov_b32_e32 v68, v73
	v_mov_b32_e32 v69, v67
	v_mov_b32_e32 v78, v21
	v_accvgpr_write_b32 a23, v89
	v_pk_fma_f32 v[62:63], v[68:69], v[6:7], v[62:63]
	v_pk_add_f32 v[60:61], v[60:61], 0 op_sel_hi:[1,0]
	v_mov_b32_dpp v78, v83 row_shr:1 row_mask:0xf bank_mask:0xf
	v_accvgpr_read_b32 v52, a30
	v_mov_b32_e32 v53, v83
	v_accvgpr_read_b32 v89, a27
	v_pk_add_f32 v[60:61], v[60:61], v[62:63]
	v_pk_mul_f32 v[62:63], v[52:53], v[78:79]
	v_accvgpr_read_b32 v88, a26
	v_mov_b32_dpp v21, v82 row_shl:1 row_mask:0xf bank_mask:0xf
	v_pk_fma_f32 v[62:63], v[82:83], v[88:89], v[62:63] op_sel_hi:[0,1,1]
	v_mov_b32_e32 v68, v83
	v_mov_b32_e32 v69, v29
	v_pk_fma_f32 v[62:63], v[68:69], v[20:21], v[62:63]
	v_mov_b32_e32 v76, v11
	v_accvgpr_read_b32 v125, a37
	v_pk_add_f32 v[60:61], v[60:61], v[62:63]
	s_mov_b64 s[0:1], 0x1410000
	v_mov_b32_dpp v76, v81 row_shr:1 row_mask:0xf bank_mask:0xf
	v_mov_b32_e32 v121, v81
	v_accvgpr_read_b32 v101, a15
	v_accvgpr_read_b32 v124, a36
	v_lshl_add_u64 v[136:137], v[134:135], 0, s[0:1]
	s_nop 1
	s_mov_b64 vcc, s[28:29]
	s_nop 0
	v_cndmask_b32_dpp v130, v60, v128, vcc quad_perm:[1,0,3,2] row_mask:0xf bank_mask:0xf
	v_cndmask_b32_dpp v131, v61, v129, vcc quad_perm:[1,0,3,2] row_mask:0xf bank_mask:0xf
	s_mov_b64 vcc, s[30:31]
	s_nop 0
	v_cndmask_b32_dpp v132, v128, v60, vcc quad_perm:[1,0,3,2] row_mask:0xf bank_mask:0xf
	v_cndmask_b32_dpp v133, v129, v61, vcc quad_perm:[1,0,3,2] row_mask:0xf bank_mask:0xf
	global_store_dwordx4 v[136:137], v[130:133], off sc0 sc1 nt
	s_nop 1
	v_pk_mul_f32 v[60:61], v[120:121], v[76:77]
	v_accvgpr_read_b32 v100, a14
	v_mov_b32_e32 v2, v35
	v_mov_b32_dpp v11, v80 row_shl:1 row_mask:0xf bank_mask:0xf
	v_pk_fma_f32 v[60:61], v[80:81], v[124:125], v[60:61] op_sel_hi:[0,1,1]
	v_pk_mov_b32 v[62:63], v[80:81], v[100:101] op_sel:[1,0]
	v_mov_b32_dpp v2, v85 row_shr:1 row_mask:0xf bank_mask:0xf
	v_mov_b32_e32 v107, v85
	v_accvgpr_read_b32 v29, a13
	v_pk_fma_f32 v[60:61], v[62:63], v[10:11], v[60:61]
	v_pk_mul_f32 v[62:63], v[106:107], v[2:3]
	v_accvgpr_read_b32 v28, a12
	v_mov_b32_dpp v35, v84 row_shl:1 row_mask:0xf bank_mask:0xf
	v_pk_fma_f32 v[62:63], v[84:85], v[28:29], v[62:63] op_sel_hi:[0,1,1]
	v_pk_mov_b32 v[68:69], v[84:85], v[122:123] op_sel:[1,0]
	v_mov_b32_e32 v92, v59
	v_pk_fma_f32 v[62:63], v[68:69], v[34:35], v[62:63]
	v_pk_add_f32 v[60:61], v[60:61], 0 op_sel_hi:[1,0]
	v_mov_b32_dpp v92, v117 row_shr:1 row_mask:0xf bank_mask:0xf
	v_mov_b32_e32 v97, v117
	v_pk_add_f32 v[60:61], v[60:61], v[62:63]
	v_pk_mul_f32 v[62:63], v[96:97], v[92:93]
	v_accvgpr_write_b32 a8, v118
	v_pk_fma_f32 v[62:63], v[116:117], v[118:119], v[62:63] op_sel_hi:[0,1,1]
	v_accvgpr_write_b32 a9, v119
	v_accvgpr_read_b32 v119, a45
	v_accvgpr_read_b32 v118, a44
	v_mov_b32_dpp v59, v116 row_shl:1 row_mask:0xf bank_mask:0xf
	v_pk_mov_b32 v[68:69], v[116:117], v[118:119] op_sel:[1,0]
	v_mov_b32_e32 v94, v57
	v_pk_fma_f32 v[62:63], v[68:69], v[58:59], v[62:63]
	s_mov_b64 s[0:1], 0x1420000
	v_pk_add_f32 v[60:61], v[60:61], v[62:63]
	v_mov_b32_dpp v94, v115 row_shr:1 row_mask:0xf bank_mask:0xf
	v_mov_b32_e32 v99, v115
	v_accvgpr_read_b32 v41, a11
	v_lshl_add_u64 v[62:63], v[54:55], 0, s[0:1]
	v_mov_b32_e32 v128, v60
	v_mov_b32_e32 v129, v61
	v_pk_mul_f32 v[60:61], v[98:99], v[94:95]
	v_accvgpr_read_b32 v40, a10
	v_mov_b32_e32 v102, v51
	v_mov_b32_dpp v57, v114 row_shl:1 row_mask:0xf bank_mask:0xf
	v_pk_fma_f32 v[60:61], v[114:115], v[40:41], v[60:61] op_sel_hi:[0,1,1]
	v_mov_b32_e32 v62, v115
	v_mov_b32_e32 v63, v101
	v_mov_b32_dpp v102, v113 row_shr:1 row_mask:0xf bank_mask:0xf
	v_mov_b32_e32 v105, v113
	v_pk_fma_f32 v[60:61], v[62:63], v[56:57], v[60:61]
	v_pk_mul_f32 v[62:63], v[104:105], v[102:103]
	v_mov_b32_dpp v51, v112 row_shl:1 row_mask:0xf bank_mask:0xf
	v_pk_fma_f32 v[62:63], v[112:113], v[4:5], v[62:63] op_sel_hi:[0,1,1]
	v_mov_b32_e32 v68, v113
	v_mov_b32_e32 v69, v123
	v_mov_b32_e32 v108, v49
	v_pk_fma_f32 v[62:63], v[68:69], v[50:51], v[62:63]
	v_pk_add_f32 v[60:61], v[60:61], 0 op_sel_hi:[1,0]
	v_mov_b32_dpp v108, v91 row_shr:1 row_mask:0xf bank_mask:0xf
	v_mov_b32_e32 v111, v91
	v_accvgpr_read_b32 v5, a3
	v_pk_add_f32 v[60:61], v[60:61], v[62:63]
	v_pk_mul_f32 v[62:63], v[110:111], v[108:109]
	v_accvgpr_read_b32 v4, a2
	v_mov_b32_dpp v49, v90 row_shl:1 row_mask:0xf bank_mask:0xf
	v_pk_fma_f32 v[62:63], v[90:91], v[4:5], v[62:63] op_sel_hi:[0,1,1]
	v_mov_b32_e32 v68, v91
	v_mov_b32_e32 v69, v119
	v_pk_fma_f32 v[62:63], v[68:69], v[48:49], v[62:63]
	s_mov_b64 s[0:1], 0x1430000
	v_pk_add_f32 v[60:61], v[60:61], v[62:63]
	v_lshl_add_u64 v[136:137], v[134:135], 0, s[0:1]
	s_nop 1
	s_mov_b64 vcc, s[28:29]
	s_nop 0
	v_cndmask_b32_dpp v130, v60, v128, vcc quad_perm:[1,0,3,2] row_mask:0xf bank_mask:0xf
	v_cndmask_b32_dpp v131, v61, v129, vcc quad_perm:[1,0,3,2] row_mask:0xf bank_mask:0xf
	s_mov_b64 vcc, s[30:31]
	s_nop 0
	v_cndmask_b32_dpp v132, v128, v60, vcc quad_perm:[1,0,3,2] row_mask:0xf bank_mask:0xf
	v_cndmask_b32_dpp v133, v129, v61, vcc quad_perm:[1,0,3,2] row_mask:0xf bank_mask:0xf
	global_store_dwordx4 v[136:137], v[130:133], off sc0 sc1 nt
	s_nop 1
	s_waitcnt vmcnt(12)
	s_waitcnt lgkmcnt(0)
	s_barrier
	v_accvgpr_read_b32 v2, a1
	v_accvgpr_read_b32 v12, a5
	ds_read_b64 v[60:61], v12
	ds_read_b64 v[62:63], v12 offset:288
	ds_read_b64 v[68:69], v12 offset:576
	ds_read_b64 v[70:71], v12 offset:1728
	ds_read_b64 v[72:73], v12 offset:2016
	ds_read_b64 v[82:83], v12 offset:2304
	ds_read_b64 v[80:81], v12 offset:3456
	ds_read_b64 v[84:85], v12 offset:3744
	ds_read_b64 v[116:117], v12 offset:4032
	ds_read_b64 v[114:115], v12 offset:5184
	ds_read_b64 v[112:113], v12 offset:5472
	ds_read_b64 v[90:91], v12 offset:5760
	ds_read_b32 v43, v2
	ds_read_b32 v19, v2 offset:288
	ds_read_b32 v39, v2 offset:576
	ds_read_b32 v25, v2 offset:1728
	ds_read_b32 v7, v2 offset:2016
	ds_read_b32 v21, v2 offset:2304
	ds_read_b32 v11, v2 offset:3456
	ds_read_b32 v35, v2 offset:3744
	ds_read_b32 v59, v2 offset:4032
	ds_read_b32 v57, v2 offset:5184
	ds_read_b32 v51, v2 offset:5472
	ds_read_b32 v49, v2 offset:5760
	s_waitcnt lgkmcnt(0)
	v_accvgpr_read_b32 v101, a23
	v_mov_b32_e32 v46, v43
	v_mov_b32_e32 v65, v61
	v_accvgpr_read_b32 v31, a25
	v_mov_b32_dpp v46, v61 row_shr:1 row_mask:0xf bank_mask:0xf
	v_pk_mul_f32 v[86:87], v[64:65], v[46:47]
	v_accvgpr_read_b32 v100, a22
	v_accvgpr_read_b32 v30, a24
	v_mov_b32_e32 v26, v19
	v_mov_b32_dpp v43, v60 row_shl:1 row_mask:0xf bank_mask:0xf
	v_pk_fma_f32 v[86:87], v[60:61], v[100:101], v[86:87] op_sel_hi:[0,1,1]
	v_pk_mov_b32 v[60:61], v[60:61], v[30:31] op_sel:[1,0]
	v_mov_b32_dpp v26, v63 row_shr:1 row_mask:0xf bank_mask:0xf
	v_mov_b32_e32 v1, v63
	v_pk_fma_f32 v[60:61], v[60:61], v[42:43], v[86:87]
	v_pk_mul_f32 v[86:87], v[0:1], v[26:27]
	v_accvgpr_read_b32 v0, a34
	v_accvgpr_mov_b32 a12, a14
	v_accvgpr_read_b32 v1, a35
	v_accvgpr_mov_b32 a13, a15
	v_mov_b32_dpp v19, v62 row_shl:1 row_mask:0xf bank_mask:0xf
	v_pk_fma_f32 v[86:87], v[62:63], v[16:17], v[86:87] op_sel_hi:[0,1,1]
	v_accvgpr_write_b32 a14, v16
	v_pk_mov_b32 v[62:63], v[62:63], v[0:1] op_sel:[1,0]
	v_mov_b32_e32 v44, v39
	v_accvgpr_write_b32 a15, v17
	v_pk_fma_f32 v[62:63], v[62:63], v[18:19], v[86:87]
	v_pk_add_f32 v[60:61], v[60:61], 0 op_sel_hi:[1,0]
	v_mov_b32_dpp v44, v69 row_shr:1 row_mask:0xf bank_mask:0xf
	v_accvgpr_read_b32 v16, a48
	v_mov_b32_e32 v17, v69
	v_accvgpr_read_b32 v67, a47
	v_pk_add_f32 v[60:61], v[60:61], v[62:63]
	v_pk_mul_f32 v[62:63], v[16:17], v[44:45]
	v_accvgpr_read_b32 v66, a46
	v_mov_b32_dpp v39, v68 row_shl:1 row_mask:0xf bank_mask:0xf
	v_pk_fma_f32 v[62:63], v[68:69], v[14:15], v[62:63] op_sel_hi:[0,1,1]
	v_pk_mov_b32 v[68:69], v[68:69], v[66:67] op_sel:[1,0]
	v_mov_b32_e32 v36, v25
	v_pk_fma_f32 v[62:63], v[68:69], v[38:39], v[62:63]
	s_mov_b64 s[0:1], 0x1800000
	v_pk_add_f32 v[60:61], v[60:61], v[62:63]
	v_mov_b32_dpp v36, v71 row_shr:1 row_mask:0xf bank_mask:0xf
	v_mov_b32_e32 v127, v71
	v_lshl_add_u64 v[62:63], v[54:55], 0, s[0:1]
	v_mov_b32_e32 v128, v60
	v_mov_b32_e32 v129, v61
	v_pk_mul_f32 v[60:61], v[126:127], v[36:37]
	v_mov_b32_e32 v12, v7
	v_mov_b32_dpp v25, v70 row_shl:1 row_mask:0xf bank_mask:0xf
	v_pk_fma_f32 v[60:61], v[70:71], v[8:9], v[60:61] op_sel_hi:[0,1,1]
	v_mov_b32_e32 v62, v71
	v_mov_b32_e32 v63, v31
	v_mov_b32_dpp v12, v73 row_shr:1 row_mask:0xf bank_mask:0xf
	v_mov_b32_e32 v75, v73
	v_pk_fma_f32 v[60:61], v[62:63], v[24:25], v[60:61]
	v_pk_mul_f32 v[62:63], v[74:75], v[12:13]
	v_mov_b32_dpp v7, v72 row_shl:1 row_mask:0xf bank_mask:0xf
	v_pk_fma_f32 v[62:63], v[72:73], v[22:23], v[62:63] op_sel_hi:[0,1,1]
	v_accvgpr_write_b32 a4, v22
	v_mov_b32_e32 v68, v73
	v_mov_b32_e32 v69, v1
	v_mov_b32_e32 v78, v21
	v_accvgpr_write_b32 a5, v23
	v_pk_fma_f32 v[62:63], v[68:69], v[6:7], v[62:63]
	v_pk_add_f32 v[60:61], v[60:61], 0 op_sel_hi:[1,0]
	v_mov_b32_dpp v78, v83 row_shr:1 row_mask:0xf bank_mask:0xf
	v_mov_b32_e32 v53, v83
	v_accvgpr_read_b32 v22, a26
	v_pk_add_f32 v[60:61], v[60:61], v[62:63]
	v_pk_mul_f32 v[62:63], v[52:53], v[78:79]
	v_accvgpr_read_b32 v23, a27
	v_mov_b32_dpp v21, v82 row_shl:1 row_mask:0xf bank_mask:0xf
	v_pk_fma_f32 v[62:63], v[82:83], v[22:23], v[62:63] op_sel_hi:[0,1,1]
	v_mov_b32_e32 v68, v83
	v_mov_b32_e32 v69, v67
	v_pk_fma_f32 v[62:63], v[68:69], v[20:21], v[62:63]
	v_mov_b32_e32 v76, v11
	v_pk_add_f32 v[60:61], v[60:61], v[62:63]
	s_mov_b64 s[0:1], 0x1810000
	v_mov_b32_dpp v76, v81 row_shr:1 row_mask:0xf bank_mask:0xf
	v_mov_b32_e32 v121, v81
	v_accvgpr_read_b32 v15, a13
	v_lshl_add_u64 v[136:137], v[134:135], 0, s[0:1]
	s_nop 1
	s_mov_b64 vcc, s[28:29]
	s_nop 0
	v_cndmask_b32_dpp v130, v60, v128, vcc quad_perm:[1,0,3,2] row_mask:0xf bank_mask:0xf
	v_cndmask_b32_dpp v131, v61, v129, vcc quad_perm:[1,0,3,2] row_mask:0xf bank_mask:0xf
	s_mov_b64 vcc, s[30:31]
	s_nop 0
	v_cndmask_b32_dpp v132, v128, v60, vcc quad_perm:[1,0,3,2] row_mask:0xf bank_mask:0xf
	v_cndmask_b32_dpp v133, v129, v61, vcc quad_perm:[1,0,3,2] row_mask:0xf bank_mask:0xf
	global_store_dwordx4 v[136:137], v[130:133], off sc0 sc1 nt
	s_nop 1
	v_pk_mul_f32 v[60:61], v[120:121], v[76:77]
	v_accvgpr_read_b32 v14, a12
	v_mov_b32_e32 v2, v35
	v_mov_b32_dpp v11, v80 row_shl:1 row_mask:0xf bank_mask:0xf
	v_pk_fma_f32 v[60:61], v[80:81], v[124:125], v[60:61] op_sel_hi:[0,1,1]
	v_pk_mov_b32 v[62:63], v[80:81], v[14:15] op_sel:[1,0]
	v_mov_b32_dpp v2, v85 row_shr:1 row_mask:0xf bank_mask:0xf
	v_mov_b32_e32 v107, v85
	v_pk_fma_f32 v[60:61], v[62:63], v[10:11], v[60:61]
	v_pk_mul_f32 v[62:63], v[106:107], v[2:3]
	v_mov_b32_dpp v35, v84 row_shl:1 row_mask:0xf bank_mask:0xf
	v_pk_fma_f32 v[62:63], v[84:85], v[28:29], v[62:63] op_sel_hi:[0,1,1]
	v_pk_mov_b32 v[68:69], v[84:85], v[122:123] op_sel:[1,0]
	v_mov_b32_e32 v92, v59
	v_pk_fma_f32 v[62:63], v[68:69], v[34:35], v[62:63]
	v_pk_add_f32 v[60:61], v[60:61], 0 op_sel_hi:[1,0]
	v_mov_b32_dpp v92, v117 row_shr:1 row_mask:0xf bank_mask:0xf
	v_mov_b32_e32 v97, v117
	v_accvgpr_read_b32 v87, a9
	v_pk_add_f32 v[60:61], v[60:61], v[62:63]
	v_pk_mul_f32 v[62:63], v[96:97], v[92:93]
	v_accvgpr_read_b32 v86, a8
	v_mov_b32_dpp v59, v116 row_shl:1 row_mask:0xf bank_mask:0xf
	v_pk_fma_f32 v[62:63], v[116:117], v[86:87], v[62:63] op_sel_hi:[0,1,1]
	v_pk_mov_b32 v[68:69], v[116:117], v[118:119] op_sel:[1,0]
	v_mov_b32_e32 v94, v57
	v_pk_fma_f32 v[62:63], v[68:69], v[58:59], v[62:63]
	s_mov_b64 s[0:1], 0x1820000
	v_pk_add_f32 v[60:61], v[60:61], v[62:63]
	v_mov_b32_dpp v94, v115 row_shr:1 row_mask:0xf bank_mask:0xf
	v_mov_b32_e32 v99, v115
	v_lshl_add_u64 v[62:63], v[54:55], 0, s[0:1]
	v_mov_b32_e32 v128, v60
	v_mov_b32_e32 v129, v61
	v_pk_mul_f32 v[60:61], v[98:99], v[94:95]
	v_mov_b32_e32 v102, v51
	v_mov_b32_dpp v57, v114 row_shl:1 row_mask:0xf bank_mask:0xf
	v_pk_fma_f32 v[60:61], v[114:115], v[40:41], v[60:61] op_sel_hi:[0,1,1]
	v_mov_b32_e32 v62, v115
	v_mov_b32_e32 v63, v15
	v_mov_b32_dpp v102, v113 row_shr:1 row_mask:0xf bank_mask:0xf
	v_mov_b32_e32 v105, v113
	v_accvgpr_read_b32 v89, a19
	v_pk_fma_f32 v[60:61], v[62:63], v[56:57], v[60:61]
	v_pk_mul_f32 v[62:63], v[104:105], v[102:103]
	v_accvgpr_read_b32 v88, a18
	v_mov_b32_dpp v51, v112 row_shl:1 row_mask:0xf bank_mask:0xf
	v_pk_fma_f32 v[62:63], v[112:113], v[88:89], v[62:63] op_sel_hi:[0,1,1]
	v_mov_b32_e32 v68, v113
	v_mov_b32_e32 v69, v123
	v_mov_b32_e32 v108, v49
	v_pk_fma_f32 v[62:63], v[68:69], v[50:51], v[62:63]
	v_pk_add_f32 v[60:61], v[60:61], 0 op_sel_hi:[1,0]
	v_mov_b32_dpp v108, v91 row_shr:1 row_mask:0xf bank_mask:0xf
	v_mov_b32_e32 v111, v91
	v_pk_add_f32 v[60:61], v[60:61], v[62:63]
	v_pk_mul_f32 v[62:63], v[110:111], v[108:109]
	v_mov_b32_dpp v49, v90 row_shl:1 row_mask:0xf bank_mask:0xf
	v_pk_fma_f32 v[62:63], v[90:91], v[4:5], v[62:63] op_sel_hi:[0,1,1]
	v_mov_b32_e32 v68, v91
	v_mov_b32_e32 v69, v119
	v_pk_fma_f32 v[62:63], v[68:69], v[48:49], v[62:63]
	s_mov_b64 s[0:1], 0x1830000
	v_pk_add_f32 v[60:61], v[60:61], v[62:63]
	v_lshl_add_u64 v[136:137], v[134:135], 0, s[0:1]
	s_nop 1
	s_mov_b64 vcc, s[28:29]
	s_nop 0
	v_cndmask_b32_dpp v130, v60, v128, vcc quad_perm:[1,0,3,2] row_mask:0xf bank_mask:0xf
	v_cndmask_b32_dpp v131, v61, v129, vcc quad_perm:[1,0,3,2] row_mask:0xf bank_mask:0xf
	s_mov_b64 vcc, s[30:31]
	s_nop 0
	v_cndmask_b32_dpp v132, v128, v60, vcc quad_perm:[1,0,3,2] row_mask:0xf bank_mask:0xf
	v_cndmask_b32_dpp v133, v129, v61, vcc quad_perm:[1,0,3,2] row_mask:0xf bank_mask:0xf
	global_store_dwordx4 v[136:137], v[130:133], off sc0 sc1 nt
	s_nop 1
	v_accvgpr_write_b32 a12, v28
	s_waitcnt vmcnt(8)
	v_accvgpr_write_b32 a13, v29
	v_mov_b64_e32 v[28:29], v[4:5]
	s_waitcnt lgkmcnt(0)
	s_barrier
	v_accvgpr_read_b32 v2, a6
	v_accvgpr_read_b32 v4, a7
	ds_read_b64 v[60:61], v2
	ds_read_b64 v[62:63], v2 offset:288
	ds_read_b64 v[68:69], v2 offset:576
	ds_read_b64 v[70:71], v2 offset:1728
	ds_read_b64 v[72:73], v2 offset:2016
	ds_read_b64 v[82:83], v2 offset:2304
	ds_read_b64 v[80:81], v2 offset:3456
	ds_read_b64 v[84:85], v2 offset:3744
	ds_read_b64 v[116:117], v2 offset:4032
	ds_read_b64 v[114:115], v2 offset:5184
	ds_read_b64 v[112:113], v2 offset:5472
	ds_read_b64 v[90:91], v2 offset:5760
	ds_read_b32 v43, v4
	ds_read_b32 v19, v4 offset:288
	ds_read_b32 v39, v4 offset:576
	ds_read_b32 v25, v4 offset:1728
	ds_read_b32 v7, v4 offset:2016
	ds_read_b32 v21, v4 offset:2304
	ds_read_b32 v11, v4 offset:3456
	ds_read_b32 v35, v4 offset:3744
	ds_read_b32 v59, v4 offset:4032
	ds_read_b32 v57, v4 offset:5184
	ds_read_b32 v51, v4 offset:5472
	ds_read_b32 v49, v4 offset:5760
	s_waitcnt lgkmcnt(0)
	v_accvgpr_read_b32 v8, a24
	v_mov_b32_e32 v46, v43
	v_mov_b32_e32 v65, v61
	v_mov_b32_e32 v26, v19
	v_mov_b32_dpp v46, v61 row_shr:1 row_mask:0xf bank_mask:0xf
	v_accvgpr_read_b32 v32, a32
	v_accvgpr_read_b32 v9, a25
	v_mov_b64_e32 v[124:125], v[40:41]
	v_pk_mul_f32 v[30:31], v[64:65], v[46:47]
	v_mov_b32_dpp v26, v63 row_shr:1 row_mask:0xf bank_mask:0xf
	v_mov_b32_e32 v33, v63
	v_accvgpr_read_b32 v4, a14
	v_accvgpr_read_b32 v41, a35
	v_mov_b32_e32 v44, v39
	v_pk_fma_f32 v[30:31], v[60:61], v[100:101], v[30:31] op_sel_hi:[0,1,1]
	v_mov_b32_dpp v43, v60 row_shl:1 row_mask:0xf bank_mask:0xf
	v_pk_mov_b32 v[46:47], v[60:61], v[8:9] op_sel:[1,0]
	v_pk_mul_f32 v[26:27], v[32:33], v[26:27]
	v_accvgpr_read_b32 v5, a15
	v_accvgpr_read_b32 v40, a34
	v_mov_b32_dpp v44, v69 row_shr:1 row_mask:0xf bank_mask:0xf
	v_mov_b32_e32 v17, v69
	v_accvgpr_read_b32 v0, a16
	v_pk_fma_f32 v[30:31], v[46:47], v[42:43], v[30:31]
	v_pk_fma_f32 v[26:27], v[62:63], v[4:5], v[26:27] op_sel_hi:[0,1,1]
	v_mov_b32_dpp v19, v62 row_shl:1 row_mask:0xf bank_mask:0xf
	v_pk_mov_b32 v[32:33], v[62:63], v[40:41] op_sel:[1,0]
	v_pk_mul_f32 v[16:17], v[16:17], v[44:45]
	v_accvgpr_read_b32 v1, a17
	v_pk_fma_f32 v[18:19], v[32:33], v[18:19], v[26:27]
	v_pk_add_f32 v[26:27], v[30:31], 0 op_sel_hi:[1,0]
	v_mov_b32_dpp v39, v68 row_shl:1 row_mask:0xf bank_mask:0xf
	v_pk_fma_f32 v[16:17], v[68:69], v[0:1], v[16:17] op_sel_hi:[0,1,1]
	v_pk_mov_b32 v[30:31], v[68:69], v[66:67] op_sel:[1,0]
	v_pk_add_f32 v[18:19], v[26:27], v[18:19]
	v_pk_fma_f32 v[16:17], v[30:31], v[38:39], v[16:17]
	v_mov_b32_e32 v36, v25
	s_mov_b64 s[0:1], 0x1c00000
	v_pk_add_f32 v[16:17], v[18:19], v[16:17]
	v_mov_b32_dpp v36, v71 row_shr:1 row_mask:0xf bank_mask:0xf
	v_mov_b32_e32 v127, v71
	v_accvgpr_read_b32 v0, a20
	v_lshl_add_u64 v[26:27], v[54:55], 0, s[0:1]
	v_mov_b32_e32 v128, v16
	v_mov_b32_e32 v129, v17
	v_mov_b32_e32 v12, v7
	v_pk_mul_f32 v[16:17], v[126:127], v[36:37]
	v_accvgpr_read_b32 v1, a21
	v_mov_b32_dpp v12, v73 row_shr:1 row_mask:0xf bank_mask:0xf
	v_pk_fma_f32 v[16:17], v[70:71], v[0:1], v[16:17] op_sel_hi:[0,1,1]
	v_mov_b32_e32 v75, v73
	v_accvgpr_read_b32 v0, a4
	v_mov_b32_e32 v78, v21
	v_pk_mul_f32 v[12:13], v[74:75], v[12:13]
	v_accvgpr_read_b32 v1, a5
	v_mov_b32_dpp v25, v70 row_shl:1 row_mask:0xf bank_mask:0xf
	v_mov_b32_dpp v7, v72 row_shl:1 row_mask:0xf bank_mask:0xf
	v_mov_b32_dpp v78, v83 row_shr:1 row_mask:0xf bank_mask:0xf
	v_mov_b32_e32 v8, v71
	v_pk_fma_f32 v[12:13], v[72:73], v[0:1], v[12:13] op_sel_hi:[0,1,1]
	v_mov_b32_e32 v5, v41
	v_mov_b32_e32 v4, v73
	v_mov_b32_e32 v53, v83
	v_pk_fma_f32 v[16:17], v[8:9], v[24:25], v[16:17]
	v_pk_fma_f32 v[6:7], v[4:5], v[6:7], v[12:13]
	v_pk_mul_f32 v[12:13], v[52:53], v[78:79]
	v_mov_b32_dpp v21, v82 row_shl:1 row_mask:0xf bank_mask:0xf
	v_pk_add_f32 v[16:17], v[16:17], 0 op_sel_hi:[1,0]
	v_pk_fma_f32 v[12:13], v[82:83], v[22:23], v[12:13] op_sel_hi:[0,1,1]
	v_mov_b32_e32 v66, v83
	v_pk_add_f32 v[6:7], v[16:17], v[6:7]
	v_pk_fma_f32 v[12:13], v[66:67], v[20:21], v[12:13]
	v_mov_b32_e32 v76, v11
	v_pk_add_f32 v[6:7], v[6:7], v[12:13]
	s_mov_b64 s[0:1], 0x1c10000
	v_mov_b32_dpp v76, v81 row_shr:1 row_mask:0xf bank_mask:0xf
	v_mov_b32_e32 v121, v81
	v_accvgpr_read_b32 v0, a36
	v_lshl_add_u64 v[136:137], v[134:135], 0, s[0:1]
	s_nop 1
	s_mov_b64 vcc, s[28:29]
	s_nop 0
	v_cndmask_b32_dpp v130, v6, v128, vcc quad_perm:[1,0,3,2] row_mask:0xf bank_mask:0xf
	v_cndmask_b32_dpp v131, v7, v129, vcc quad_perm:[1,0,3,2] row_mask:0xf bank_mask:0xf
	s_mov_b64 vcc, s[30:31]
	s_nop 0
	v_cndmask_b32_dpp v132, v128, v6, vcc quad_perm:[1,0,3,2] row_mask:0xf bank_mask:0xf
	v_cndmask_b32_dpp v133, v129, v7, vcc quad_perm:[1,0,3,2] row_mask:0xf bank_mask:0xf
	global_store_dwordx4 v[136:137], v[130:133], off sc0 sc1 nt
	s_nop 1
	v_mov_b32_e32 v2, v35
	v_pk_mul_f32 v[6:7], v[120:121], v[76:77]
	v_accvgpr_read_b32 v1, a37
	v_mov_b32_dpp v2, v85 row_shr:1 row_mask:0xf bank_mask:0xf
	v_pk_fma_f32 v[6:7], v[80:81], v[0:1], v[6:7] op_sel_hi:[0,1,1]
	v_mov_b32_e32 v107, v85
	v_accvgpr_read_b32 v0, a12
	v_mov_b32_e32 v92, v59
	v_pk_mul_f32 v[2:3], v[106:107], v[2:3]
	v_accvgpr_read_b32 v1, a13
	v_mov_b32_dpp v11, v80 row_shl:1 row_mask:0xf bank_mask:0xf
	v_mov_b32_dpp v35, v84 row_shl:1 row_mask:0xf bank_mask:0xf
	v_mov_b32_dpp v92, v117 row_shr:1 row_mask:0xf bank_mask:0xf
	v_pk_mov_b32 v[8:9], v[80:81], v[14:15] op_sel:[1,0]
	v_pk_fma_f32 v[2:3], v[84:85], v[0:1], v[2:3] op_sel_hi:[0,1,1]
	v_pk_mov_b32 v[4:5], v[84:85], v[122:123] op_sel:[1,0]
	v_mov_b32_e32 v97, v117
	v_pk_fma_f32 v[6:7], v[8:9], v[10:11], v[6:7]
	v_pk_fma_f32 v[0:1], v[4:5], v[34:35], v[2:3]
	v_pk_mul_f32 v[2:3], v[96:97], v[92:93]
	v_mov_b32_dpp v59, v116 row_shl:1 row_mask:0xf bank_mask:0xf
	v_pk_add_f32 v[6:7], v[6:7], 0 op_sel_hi:[1,0]
	v_pk_fma_f32 v[2:3], v[116:117], v[86:87], v[2:3] op_sel_hi:[0,1,1]
	v_pk_mov_b32 v[4:5], v[116:117], v[118:119] op_sel:[1,0]
	v_pk_add_f32 v[0:1], v[6:7], v[0:1]
	v_pk_fma_f32 v[2:3], v[4:5], v[58:59], v[2:3]
	v_mov_b32_e32 v94, v57
	v_pk_add_f32 v[0:1], v[0:1], v[2:3]
	s_mov_b64 s[0:1], 0x1c20000
	v_mov_b32_dpp v94, v115 row_shr:1 row_mask:0xf bank_mask:0xf
	v_mov_b32_e32 v102, v51
	v_mov_b32_e32 v99, v115
	v_lshl_add_u64 v[2:3], v[54:55], 0, s[0:1]
	v_mov_b32_e32 v128, v0
	v_mov_b32_e32 v129, v1
	v_mov_b32_dpp v102, v113 row_shr:1 row_mask:0xf bank_mask:0xf
	v_pk_mul_f32 v[0:1], v[98:99], v[94:95]
	v_mov_b32_e32 v105, v113
	v_mov_b32_dpp v57, v114 row_shl:1 row_mask:0xf bank_mask:0xf
	v_pk_fma_f32 v[0:1], v[114:115], v[124:125], v[0:1] op_sel_hi:[0,1,1]
	v_mov_b32_e32 v14, v115
	v_pk_mul_f32 v[2:3], v[104:105], v[102:103]
	v_mov_b32_dpp v51, v112 row_shl:1 row_mask:0xf bank_mask:0xf
	v_mov_b32_e32 v108, v49
	v_pk_fma_f32 v[0:1], v[14:15], v[56:57], v[0:1]
	v_pk_fma_f32 v[2:3], v[112:113], v[88:89], v[2:3] op_sel_hi:[0,1,1]
	v_mov_b32_e32 v122, v113
	v_mov_b32_dpp v108, v91 row_shr:1 row_mask:0xf bank_mask:0xf
	v_pk_add_f32 v[0:1], v[0:1], 0 op_sel_hi:[1,0]
	v_pk_fma_f32 v[2:3], v[122:123], v[50:51], v[2:3]
	v_mov_b32_e32 v111, v91
	v_pk_add_f32 v[0:1], v[0:1], v[2:3]
	v_pk_mul_f32 v[2:3], v[110:111], v[108:109]
	v_mov_b32_dpp v49, v90 row_shl:1 row_mask:0xf bank_mask:0xf
	v_pk_fma_f32 v[2:3], v[90:91], v[28:29], v[2:3] op_sel_hi:[0,1,1]
	v_mov_b32_e32 v118, v91
	v_pk_fma_f32 v[2:3], v[118:119], v[48:49], v[2:3]
	s_mov_b64 s[0:1], 0x1c30000
	v_pk_add_f32 v[0:1], v[0:1], v[2:3]
	v_lshl_add_u64 v[136:137], v[134:135], 0, s[0:1]
	s_nop 1
	s_mov_b64 vcc, s[28:29]
	s_nop 0
	v_cndmask_b32_dpp v130, v0, v128, vcc quad_perm:[1,0,3,2] row_mask:0xf bank_mask:0xf
	v_cndmask_b32_dpp v131, v1, v129, vcc quad_perm:[1,0,3,2] row_mask:0xf bank_mask:0xf
	s_mov_b64 vcc, s[30:31]
	s_nop 0
	v_cndmask_b32_dpp v132, v128, v0, vcc quad_perm:[1,0,3,2] row_mask:0xf bank_mask:0xf
	v_cndmask_b32_dpp v133, v129, v1, vcc quad_perm:[1,0,3,2] row_mask:0xf bank_mask:0xf
	global_store_dwordx4 v[136:137], v[130:133], off sc0 sc1 nt
	s_nop 1
	s_endpgm
